# P7/P8 K-loop load segments: LDS-DMA group issued before the last ds_read_b128 run (more flight time per DMA)
# baseline (speedup 1.0000x reference)
; #define PG8_STAGE(bufoff, gbase, voff) do { if constexpr (!(Sched::CRIP & 2)) _Pragma("unroll") for (int _i = 0; _i < 2; ++_i) { unsigned _o = (voff)[_i]; asm volatile("" : "+v"(_o)); \
;         __builtin_amdgcn_global_load_lds((const unsigned*)((const char*)(gbase) + _o), (LAS unsigned*)(lds + (bufoff) + ldsw + _i * 8192), 16, 0, 0); } } while (0)
; #define PG8_LDA(dst, b, h) do { if constexpr (!(Sched::CRIP & 4)) _Pragma("unroll") for (int m = 0; m < 4; ++m) dst[m] = PG8_CAT(*(const LAS i32x4*)(lds + PG8_SA(b, h) + aoff + m * 2048), *(const LAS i32x4*)(lds + PG8_SA(b, h) + aoff + m * 2048 + 1024)); } while (0)
; #define PG8_LDB(dst, b, h) do { if constexpr (!(Sched::CRIP & 4)) _Pragma("unroll") for (int n = 0; n < 2; ++n) dst[n] = PG8_CAT(*(const LAS i32x4*)(lds + PG8_SB(b, h) + boff + n * 2048), *(const LAS i32x4*)(lds + PG8_SB(b, h) + boff + n * 2048 + 1024)); } while (0)
; #define PG8_WAIT_V(n) asm volatile("s_waitcnt vmcnt(" #n ")" ::: "memory")
; #define PG8_WAIT_L(n) asm volatile("s_waitcnt lgkmcnt(" #n ")" ::: "memory")
; #define PG8_BAR __builtin_amdgcn_s_barrier()
; #define PG8_SCHED __builtin_amdgcn_sched_barrier(0)
; template <class Epi, class Sched>
; __device__ __forceinline__ void gemm_phase(LAS unsigned char* lds, const Sched& S, const Epi& E) {
;     ...
;             PG8_LDB(B0, 0, 0); PG8_LDB(B1, 0, 1); PG8_SCHED; PG8_LDA(At, 0, 0); PG8_STAGE(PG8_SA(1, 1), a1, vA[1]);
;             PG8_WAIT_V(8); PG8_WAIT_L(0); PG8_BAR; PG8_MMA(0, 0, At, B0); PG8_MMA(0, 1, At, B1); PG8_BAR2; PG8_SCHED;
;             if constexpr (Sched::GATHER) { if (last && has_next) {
;                 int tz = threadIdx.x; asm volatile("" : "+v"(tz));
; #pragma unroll
;                 for (int i = 0; i < 2; ++i) { int R, C; stage_rc(tz * 16 + i * 8192, R, C);
; #pragma unroll
;                     for (int h = 0; h < 2; ++h) vA[h][i] = (unsigned)(lidx[h * HALF + R] * RP + C * 2); } } }
;             PG8_LDA(At, 0, 1); PG8_STAGE(PG8_SB(0, 0), b2, voffB); PG8_STAGE(PG8_SB(0, 1), b2 + hstep, voffB); PG8_STAGE(PG8_SA(0, 0), a2, vA[0]);
;             PG8_WAIT_V(8); PG8_WAIT_L(0); PG8_BAR; PG8_MMA(1, 0, At, B0); PG8_MMA(1, 1, At, B1); PG8_BAR2; PG8_SCHED;
.LBB0_731:
	s_or_b64 exec, exec, s[34:35]
	s_lshl_b32 s18, s19, 7
	s_add_i32 s21, s18, 0x80
	s_and_b32 s21, s21, 0x780
	s_add_u32 s46, s58, s21
	s_addc_u32 s47, s59, 0
	s_add_i32 s21, s18, 0x100
	s_and_b32 s21, s21, 0x780
	v_add_u32_e32 v3, s92, v196
	s_add_u32 s40, s58, s21
	ds_read_b128 v[4:7], v3
	ds_read_b128 v[8:11], v3 offset:1024
	ds_read_b128 v[12:15], v3 offset:2048
	ds_read_b128 v[16:19], v3 offset:3072
	v_add_u32_e32 v3, s93, v196
	s_addc_u32 s41, s59, 0
	ds_read_b128 v[20:23], v3
	ds_read_b128 v[24:27], v3 offset:1024
	ds_read_b128 v[204:207], v3 offset:2048
	ds_read_b128 v[208:211], v3 offset:3072
	s_add_u32 s42, s28, s21
	s_addc_u32 s43, s29, 0
	s_add_i32 s21, s18, 0x180
	s_and_b32 s18, s21, 0x780
	s_add_u32 s34, s58, s18
	s_addc_u32 s35, s59, 0
	s_add_u32 s36, s28, s18
	s_addc_u32 s37, s29, 0
	v_mov_b32_e32 v3, v193
	s_add_i32 s27, s39, 0xc000
	s_mov_b32 m0, s27
	s_add_i32 s62, s39, 0xe000
	global_load_lds_dwordx4 v3, s[46:47]
	v_mov_b32_e32 v3, v195
	s_mov_b32 m0, s62
	s_nop 0
	global_load_lds_dwordx4 v3, s[46:47]
	ds_read_b128 v[48:51], v200
	ds_read_b128 v[52:55], v200 offset:1024
	ds_read_b128 v[56:59], v200 offset:2048
	ds_read_b128 v[60:63], v200 offset:3072
	ds_read_b128 v[64:67], v200 offset:4096
	ds_read_b128 v[68:71], v200 offset:5120
	ds_read_b128 v[82:85], v200 offset:6144
	ds_read_b128 v[86:89], v200 offset:7168
	s_waitcnt vmcnt(16)
	s_waitcnt lgkmcnt(0)
	s_barrier
	s_setprio 1
	s_waitcnt lgkmcnt(0)
	s_nop 1
	v_mfma_scale_f32_16x16x128_f8f6f4 v[178:181], v[4:11], v[48:55], 0, v191, v191 op_sel_hi:[0,0,0]
	v_mfma_scale_f32_16x16x128_f8f6f4 v[170:173], v[12:19], v[48:55], 0, v191, v191 op_sel_hi:[0,0,0]
	v_mfma_scale_f32_16x16x128_f8f6f4 v[162:165], v[4:11], v[56:63], 0, v191, v191 op_sel_hi:[0,0,0]
	v_mfma_scale_f32_16x16x128_f8f6f4 v[154:157], v[12:19], v[56:63], 0, v191, v191 op_sel_hi:[0,0,0]
	v_mfma_scale_f32_16x16x128_f8f6f4 v[146:149], v[4:11], v[64:71], 0, v191, v191 op_sel_hi:[0,0,0]
	v_mfma_scale_f32_16x16x128_f8f6f4 v[138:141], v[12:19], v[64:71], 0, v191, v191 op_sel_hi:[0,0,0]
	v_mfma_scale_f32_16x16x128_f8f6f4 v[130:133], v[4:11], v[82:89], 0, v191, v191 op_sel_hi:[0,0,0]
	v_mfma_scale_f32_16x16x128_f8f6f4 v[122:125], v[12:19], v[82:89], 0, v191, v191 op_sel_hi:[0,0,0]
	s_setprio 0
	s_setprio 1
	s_nop 1
	v_mfma_scale_f32_16x16x128_f8f6f4 v[182:185], v[20:27], v[48:55], 0, v191, v191 op_sel_hi:[0,0,0]
	v_mfma_scale_f32_16x16x128_f8f6f4 v[174:177], v[204:211], v[48:55], 0, v191, v191 op_sel_hi:[0,0,0]
	v_mfma_scale_f32_16x16x128_f8f6f4 v[166:169], v[20:27], v[56:63], 0, v191, v191 op_sel_hi:[0,0,0]
	v_mfma_scale_f32_16x16x128_f8f6f4 v[158:161], v[204:211], v[56:63], 0, v191, v191 op_sel_hi:[0,0,0]
	v_mfma_scale_f32_16x16x128_f8f6f4 v[150:153], v[20:27], v[64:71], 0, v191, v191 op_sel_hi:[0,0,0]
	v_mfma_scale_f32_16x16x128_f8f6f4 v[142:145], v[204:211], v[64:71], 0, v191, v191 op_sel_hi:[0,0,0]
	v_mfma_scale_f32_16x16x128_f8f6f4 v[134:137], v[20:27], v[82:89], 0, v191, v191 op_sel_hi:[0,0,0]
	v_mfma_scale_f32_16x16x128_f8f6f4 v[126:129], v[204:211], v[82:89], 0, v191, v191 op_sel_hi:[0,0,0]
	s_setprio 0
	s_barrier
	v_mov_b32_e32 v3, v1
	s_add_i32 s18, s92, s61
	s_mov_b32 m0, s18
	s_nop 0
	global_load_lds_dwordx4 v3, s[42:43]
	v_mov_b32_e32 v3, v190
	s_add_i32 m0, s18, 0x2000
	s_nop 0
	global_load_lds_dwordx4 v3, s[42:43]
	s_add_u32 s42, s42, 0x40000
	s_addc_u32 s43, s43, 0
	v_mov_b32_e32 v3, v1
	s_add_i32 s18, s93, s61
	s_mov_b32 m0, s18
	s_nop 0
	global_load_lds_dwordx4 v3, s[42:43]
	v_mov_b32_e32 v3, v190
	s_add_i32 m0, s18, 0x2000
	s_nop 0
	global_load_lds_dwordx4 v3, s[42:43]
	v_mov_b32_e32 v3, v192
	s_mov_b32 m0, s39
	s_nop 0
	global_load_lds_dwordx4 v3, s[40:41]
	v_mov_b32_e32 v3, v194
	s_mov_b32 m0, s67
	s_nop 0
	global_load_lds_dwordx4 v3, s[40:41]
	ds_read_b128 v[218:221], v200 offset:23552
	ds_read_b128 v[214:217], v200 offset:22528
	ds_read_b128 v[226:229], v200 offset:21504
	ds_read_b128 v[222:225], v200 offset:20480
	ds_read_b128 v[234:237], v200 offset:19456
	ds_read_b128 v[230:233], v200 offset:18432
	ds_read_b128 v[242:245], v200 offset:17408
	ds_read_b128 v[238:241], v200 offset:16384
	s_waitcnt vmcnt(16)
	s_waitcnt lgkmcnt(0)
	s_barrier
	s_setprio 1
	s_waitcnt lgkmcnt(0)
	s_nop 1
	v_mfma_scale_f32_16x16x128_f8f6f4 v[118:121], v[4:11], v[238:245], 0, v191, v191 op_sel_hi:[0,0,0]
	v_mfma_scale_f32_16x16x128_f8f6f4 v[110:113], v[12:19], v[238:245], 0, v191, v191 op_sel_hi:[0,0,0]
	v_mfma_scale_f32_16x16x128_f8f6f4 v[98:101], v[4:11], v[230:237], 0, v191, v191 op_sel_hi:[0,0,0]
	v_mfma_scale_f32_16x16x128_f8f6f4 v[90:93], v[12:19], v[230:237], 0, v191, v191 op_sel_hi:[0,0,0]
	v_mfma_scale_f32_16x16x128_f8f6f4 v[82:85], v[4:11], v[222:229], 0, v191, v191 op_sel_hi:[0,0,0]
	v_mfma_scale_f32_16x16x128_f8f6f4 v[66:69], v[12:19], v[222:229], 0, v191, v191 op_sel_hi:[0,0,0]
	v_mfma_scale_f32_16x16x128_f8f6f4 v[58:61], v[4:11], v[214:221], 0, v191, v191 op_sel_hi:[0,0,0]
	v_mfma_scale_f32_16x16x128_f8f6f4 v[50:53], v[12:19], v[214:221], 0, v191, v191 op_sel_hi:[0,0,0]
	s_setprio 0
	s_setprio 1
	s_nop 1
	v_mfma_scale_f32_16x16x128_f8f6f4 v[106:109], v[20:27], v[238:245], 0, v191, v191 op_sel_hi:[0,0,0]
	v_mfma_scale_f32_16x16x128_f8f6f4 v[114:117], v[204:211], v[238:245], 0, v191, v191 op_sel_hi:[0,0,0]
	v_mfma_scale_f32_16x16x128_f8f6f4 v[102:105], v[20:27], v[230:237], 0, v191, v191 op_sel_hi:[0,0,0]
	v_mfma_scale_f32_16x16x128_f8f6f4 v[94:97], v[204:211], v[230:237], 0, v191, v191 op_sel_hi:[0,0,0]
	v_mfma_scale_f32_16x16x128_f8f6f4 v[86:89], v[20:27], v[222:229], 0, v191, v191 op_sel_hi:[0,0,0]
	v_mfma_scale_f32_16x16x128_f8f6f4 v[70:73], v[204:211], v[222:229], 0, v191, v191 op_sel_hi:[0,0,0]
	v_mfma_scale_f32_16x16x128_f8f6f4 v[62:65], v[20:27], v[214:221], 0, v191, v191 op_sel_hi:[0,0,0]
	v_mfma_scale_f32_16x16x128_f8f6f4 v[54:57], v[204:211], v[214:221], 0, v191, v191 op_sel_hi:[0,0,0]
	s_setprio 0
	s_barrier
; #define PG8_STAGE(bufoff, gbase, voff) do { if constexpr (!(Sched::CRIP & 2)) _Pragma("unroll") for (int _i = 0; _i < 2; ++_i) { unsigned _o = (voff)[_i]; asm volatile("" : "+v"(_o)); \
;         __builtin_amdgcn_global_load_lds((const unsigned*)((const char*)(gbase) + _o), (LAS unsigned*)(lds + (bufoff) + ldsw + _i * 8192), 16, 0, 0); } } while (0)
; #define PG8_LDA(dst, b, h) do { if constexpr (!(Sched::CRIP & 4)) _Pragma("unroll") for (int m = 0; m < 4; ++m) dst[m] = PG8_CAT(*(const LAS i32x4*)(lds + PG8_SA(b, h) + aoff + m * 2048), *(const LAS i32x4*)(lds + PG8_SA(b, h) + aoff + m * 2048 + 1024)); } while (0)
; #define PG8_LDB(dst, b, h) do { if constexpr (!(Sched::CRIP & 4)) _Pragma("unroll") for (int n = 0; n < 2; ++n) dst[n] = PG8_CAT(*(const LAS i32x4*)(lds + PG8_SB(b, h) + boff + n * 2048), *(const LAS i32x4*)(lds + PG8_SB(b, h) + boff + n * 2048 + 1024)); } while (0)
; #define PG8_WAIT_V(n) asm volatile("s_waitcnt vmcnt(" #n ")" ::: "memory")
; #define PG8_WAIT_L(n) asm volatile("s_waitcnt lgkmcnt(" #n ")" ::: "memory")
; #define PG8_BAR __builtin_amdgcn_s_barrier()
; #define PG8_SCHED __builtin_amdgcn_sched_barrier(0)
; template <class Epi, class Sched>
; __device__ __forceinline__ void gemm_phase(LAS unsigned char* lds, const Sched& S, const Epi& E) {
;     ...
;             PG8_LDB(B0, 1, 0); PG8_LDB(B1, 1, 1); PG8_SCHED; PG8_LDA(At, 1, 0); PG8_STAGE(PG8_SA(0, 1), a2, vA[1]);
;             PG8_WAIT_V(8); PG8_WAIT_L(0); PG8_BAR; PG8_MMA(0, 0, At, B0); PG8_MMA(0, 1, At, B1); PG8_BAR2; PG8_SCHED;
;             PG8_LDA(At, 1, 1); PG8_STAGE(PG8_SB(1, 0), b3, voffB); PG8_STAGE(PG8_SB(1, 1), b3 + hstep, voffB); PG8_STAGE(PG8_SA(1, 0), a3, vA[0]);
;             PG8_WAIT_V(8); PG8_WAIT_L(0); PG8_BAR; PG8_MMA(1, 0, At, B0); PG8_MMA(1, 1, At, B1); PG8_BAR2; PG8_SCHED;
;             if constexpr (Sched::GATHER) { if (t == 0 && has_next && tid < 256) lidx[tid] = (tid < nxt.avalid) ? gi : 0; }
	s_add_i32 s18, 0, 0x18000
	s_add_i32 s42, 0, 0x1c000
	v_add_u32_e32 v43, s18, v196
	v_add_u32_e32 v44, s42, v196
	ds_read_b128 v[4:7], v43
	ds_read_b128 v[8:11], v43 offset:1024
	ds_read_b128 v[12:15], v43 offset:2048
	ds_read_b128 v[16:19], v43 offset:3072
	ds_read_b128 v[20:23], v44
	ds_read_b128 v[24:27], v44 offset:1024
	ds_read_b128 v[204:207], v44 offset:2048
	ds_read_b128 v[208:211], v44 offset:3072
	v_mov_b32_e32 v3, v193
	s_mov_b32 m0, s68
	s_nop 0
	global_load_lds_dwordx4 v3, s[40:41]
	v_mov_b32_e32 v3, v195
	s_mov_b32 m0, s69
	s_nop 0
	global_load_lds_dwordx4 v3, s[40:41]
	ds_read_b128 v[214:217], v200 offset:32768
	ds_read_b128 v[218:221], v200 offset:33792
	ds_read_b128 v[222:225], v200 offset:34816
	ds_read_b128 v[226:229], v200 offset:35840
	ds_read_b128 v[230:233], v200 offset:36864
	ds_read_b128 v[234:237], v200 offset:37888
	ds_read_b128 v[238:241], v200 offset:38912
	ds_read_b128 v[242:245], v200 offset:39936
	s_waitcnt vmcnt(8)
	s_waitcnt lgkmcnt(0)
	s_barrier
	s_setprio 1
	s_waitcnt lgkmcnt(0)
	s_nop 1
	v_mfma_scale_f32_16x16x128_f8f6f4 v[178:181], v[4:11], v[214:221], v[178:181], v191, v191 op_sel_hi:[0,0,0]
	v_mfma_scale_f32_16x16x128_f8f6f4 v[170:173], v[12:19], v[214:221], v[170:173], v191, v191 op_sel_hi:[0,0,0]
	v_mfma_scale_f32_16x16x128_f8f6f4 v[162:165], v[4:11], v[222:229], v[162:165], v191, v191 op_sel_hi:[0,0,0]
	v_mfma_scale_f32_16x16x128_f8f6f4 v[154:157], v[12:19], v[222:229], v[154:157], v191, v191 op_sel_hi:[0,0,0]
	v_mfma_scale_f32_16x16x128_f8f6f4 v[146:149], v[4:11], v[230:237], v[146:149], v191, v191 op_sel_hi:[0,0,0]
	v_mfma_scale_f32_16x16x128_f8f6f4 v[138:141], v[12:19], v[230:237], v[138:141], v191, v191 op_sel_hi:[0,0,0]
	v_mfma_scale_f32_16x16x128_f8f6f4 v[130:133], v[4:11], v[238:245], v[130:133], v191, v191 op_sel_hi:[0,0,0]
	v_mfma_scale_f32_16x16x128_f8f6f4 v[122:125], v[12:19], v[238:245], v[122:125], v191, v191 op_sel_hi:[0,0,0]
	s_setprio 0
	s_setprio 1
	s_nop 1
	v_mfma_scale_f32_16x16x128_f8f6f4 v[182:185], v[20:27], v[214:221], v[182:185], v191, v191 op_sel_hi:[0,0,0]
	v_mfma_scale_f32_16x16x128_f8f6f4 v[174:177], v[204:211], v[214:221], v[174:177], v191, v191 op_sel_hi:[0,0,0]
	v_mfma_scale_f32_16x16x128_f8f6f4 v[166:169], v[20:27], v[222:229], v[166:169], v191, v191 op_sel_hi:[0,0,0]
	v_mfma_scale_f32_16x16x128_f8f6f4 v[158:161], v[204:211], v[222:229], v[158:161], v191, v191 op_sel_hi:[0,0,0]
	v_mfma_scale_f32_16x16x128_f8f6f4 v[150:153], v[20:27], v[230:237], v[150:153], v191, v191 op_sel_hi:[0,0,0]
	v_mfma_scale_f32_16x16x128_f8f6f4 v[142:145], v[204:211], v[230:237], v[142:145], v191, v191 op_sel_hi:[0,0,0]
	v_mfma_scale_f32_16x16x128_f8f6f4 v[134:137], v[20:27], v[238:245], v[134:137], v191, v191 op_sel_hi:[0,0,0]
	v_mfma_scale_f32_16x16x128_f8f6f4 v[126:129], v[204:211], v[238:245], v[126:129], v191, v191 op_sel_hi:[0,0,0]
	s_setprio 0
	s_barrier
	v_mov_b32_e32 v3, v1
	s_add_i32 s40, s18, s61
	s_mov_b32 m0, s40
	s_add_i32 s41, s40, 0x2000
	global_load_lds_dwordx4 v3, s[36:37]
	v_mov_b32_e32 v3, v190
	s_mov_b32 m0, s41
	s_nop 0
	global_load_lds_dwordx4 v3, s[36:37]
	s_add_u32 s36, s36, 0x40000
	s_addc_u32 s37, s37, 0
	v_mov_b32_e32 v3, v1
	s_add_i32 s42, s42, s61
	s_mov_b32 m0, s42
	s_add_i32 s43, s42, 0x2000
	global_load_lds_dwordx4 v3, s[36:37]
	v_mov_b32_e32 v3, v190
	s_mov_b32 m0, s43
	s_nop 0
	global_load_lds_dwordx4 v3, s[36:37]
	v_mov_b32_e32 v3, v192
	s_mov_b32 m0, s70
	s_nop 0
	global_load_lds_dwordx4 v3, s[34:35]
	v_mov_b32_e32 v3, v194
	s_mov_b32 m0, s71
	s_nop 0
	global_load_lds_dwordx4 v3, s[34:35]
	ds_read_b128 v[214:217], v200 offset:49152
	ds_read_b128 v[218:221], v200 offset:50176
	ds_read_b128 v[222:225], v200 offset:51200
	ds_read_b128 v[226:229], v200 offset:52224
	ds_read_b128 v[230:233], v200 offset:53248
	ds_read_b128 v[234:237], v200 offset:54272
	ds_read_b128 v[238:241], v200 offset:55296
	ds_read_b128 v[242:245], v200 offset:56320
	s_waitcnt vmcnt(8)
	s_waitcnt lgkmcnt(0)
	s_barrier
	s_setprio 1
	s_waitcnt lgkmcnt(0)
	s_nop 1
	v_mfma_scale_f32_16x16x128_f8f6f4 v[118:121], v[4:11], v[214:221], v[118:121], v191, v191 op_sel_hi:[0,0,0]
	v_mfma_scale_f32_16x16x128_f8f6f4 v[110:113], v[12:19], v[214:221], v[110:113], v191, v191 op_sel_hi:[0,0,0]
	v_mfma_scale_f32_16x16x128_f8f6f4 v[98:101], v[4:11], v[222:229], v[98:101], v191, v191 op_sel_hi:[0,0,0]
	v_mfma_scale_f32_16x16x128_f8f6f4 v[90:93], v[12:19], v[222:229], v[90:93], v191, v191 op_sel_hi:[0,0,0]
	v_mfma_scale_f32_16x16x128_f8f6f4 v[82:85], v[4:11], v[230:237], v[82:85], v191, v191 op_sel_hi:[0,0,0]
	v_mfma_scale_f32_16x16x128_f8f6f4 v[66:69], v[12:19], v[230:237], v[66:69], v191, v191 op_sel_hi:[0,0,0]
	v_mfma_scale_f32_16x16x128_f8f6f4 v[58:61], v[4:11], v[238:245], v[58:61], v191, v191 op_sel_hi:[0,0,0]
	v_mfma_scale_f32_16x16x128_f8f6f4 v[50:53], v[12:19], v[238:245], v[50:53], v191, v191 op_sel_hi:[0,0,0]
	s_setprio 0
	s_setprio 1
	s_nop 1
	v_mfma_scale_f32_16x16x128_f8f6f4 v[106:109], v[20:27], v[214:221], v[106:109], v191, v191 op_sel_hi:[0,0,0]
	v_mfma_scale_f32_16x16x128_f8f6f4 v[114:117], v[204:211], v[214:221], v[114:117], v191, v191 op_sel_hi:[0,0,0]
	v_mfma_scale_f32_16x16x128_f8f6f4 v[102:105], v[20:27], v[222:229], v[102:105], v191, v191 op_sel_hi:[0,0,0]
	v_mfma_scale_f32_16x16x128_f8f6f4 v[94:97], v[204:211], v[222:229], v[94:97], v191, v191 op_sel_hi:[0,0,0]
	v_mfma_scale_f32_16x16x128_f8f6f4 v[86:89], v[20:27], v[230:237], v[86:89], v191, v191 op_sel_hi:[0,0,0]
	v_mfma_scale_f32_16x16x128_f8f6f4 v[70:73], v[204:211], v[230:237], v[70:73], v191, v191 op_sel_hi:[0,0,0]
	v_mfma_scale_f32_16x16x128_f8f6f4 v[62:65], v[20:27], v[238:245], v[62:65], v191, v191 op_sel_hi:[0,0,0]
	v_mfma_scale_f32_16x16x128_f8f6f4 v[54:57], v[204:211], v[238:245], v[54:57], v191, v191 op_sel_hi:[0,0,0]
	s_setprio 0
	s_barrier
	s_and_saveexec_b64 s[34:35], s[30:31]
	s_cbranch_execz .LBB0_733
	v_cmp_gt_i32_e32 vcc, s90, v0
	s_waitcnt vmcnt(8)
	s_nop 0
	v_cndmask_b32_e32 v2, 0, v2, vcc
	ds_write_b32 v197, v2

; #define PG8_STAGE(bufoff, gbase, voff) do { if constexpr (!(Sched::CRIP & 2)) _Pragma("unroll") for (int _i = 0; _i < 2; ++_i) { unsigned _o = (voff)[_i]; asm volatile("" : "+v"(_o)); \
;         __builtin_amdgcn_global_load_lds((const unsigned*)((const char*)(gbase) + _o), (LAS unsigned*)(lds + (bufoff) + ldsw + _i * 8192), 16, 0, 0); } } while (0)
; #define PG8_LDA(dst, b, h) do { if constexpr (!(Sched::CRIP & 4)) _Pragma("unroll") for (int m = 0; m < 4; ++m) dst[m] = PG8_CAT(*(const LAS i32x4*)(lds + PG8_SA(b, h) + aoff + m * 2048), *(const LAS i32x4*)(lds + PG8_SA(b, h) + aoff + m * 2048 + 1024)); } while (0)
; template <class Epi, class Sched>
; __device__ __forceinline__ void gemm_phase(LAS unsigned char* lds, const Sched& S, const Epi& E) {
;     ...
;             const char* a1 = cA + PG8_KT(crot, t + 1);
;             const char* a2 = last ? nA + PG8_KT(nrot, 0) : cA + PG8_KT(crot, t + 2); const char* b2 = last ? nB + PG8_KT(nrot, 0) : cB + PG8_KT(crot, t + 2);
;             const char* a3 = last ? nA + PG8_KT(nrot, 1) : cA + PG8_KT(crot, t + 3); const char* b3 = last ? nB + PG8_KT(nrot, 1) : cB + PG8_KT(crot, t + 3);
;             int gi = 0;
;             if constexpr (Sched::GATHER) { if (t == 0 && has_next && tid < 256) gi = nxt.aidx[tid]; }
;             PG8_LDB(B0, 0, 0); PG8_LDB(B1, 0, 1); PG8_SCHED; PG8_LDA(At, 0, 0); PG8_STAGE(PG8_SA(1, 1), a1, vA[1]);
;             PG8_WAIT_V(8); PG8_WAIT_L(0); PG8_BAR; PG8_MMA(0, 0, At, B0); PG8_MMA(0, 1, At, B1); PG8_BAR2; PG8_SCHED;
;             if constexpr (Sched::GATHER) { if (last && has_next) {
;                 int tz = threadIdx.x; asm volatile("" : "+v"(tz));
; #pragma unroll
;                 for (int i = 0; i < 2; ++i) { int R, C; stage_rc(tz * 16 + i * 8192, R, C);
; #pragma unroll
;                     for (int h = 0; h < 2; ++h) vA[h][i] = (unsigned)(lidx[h * HALF + R] * RP + C * 2); } } }
;             PG8_LDA(At, 0, 1); PG8_STAGE(PG8_SB(0, 0), b2, voffB); PG8_STAGE(PG8_SB(0, 1), b2 + hstep, voffB); PG8_STAGE(PG8_SA(0, 0), a2, vA[0]);
;             PG8_WAIT_V(8); PG8_WAIT_L(0); PG8_BAR; PG8_MMA(1, 0, At, B0); PG8_MMA(1, 1, At, B1); PG8_BAR2; PG8_SCHED;
;             PG8_LDB(B0, 1, 0); PG8_LDB(B1, 1, 1); PG8_SCHED; PG8_LDA(At, 1, 0); PG8_STAGE(PG8_SA(0, 1), a2, vA[1]);
;             PG8_WAIT_V(8); PG8_WAIT_L(0); PG8_BAR; PG8_MMA(0, 0, At, B0); PG8_MMA(0, 1, At, B1); PG8_BAR2; PG8_SCHED;
.LBB0_734:
	s_add_i32 s30, s21, 0x80
	s_and_b32 s53, s30, 0x780
	s_and_b64 s[30:31], s[34:35], exec
	s_cselect_b32 s31, s19, s53
	s_cselect_b32 s30, 0, 0
	s_add_u32 s36, s58, s31
	s_addc_u32 s37, s59, s30
	s_add_u32 s53, s28, s53
	s_addc_u32 s54, s29, 0
	s_and_b64 s[30:31], s[34:35], exec
	s_cselect_b32 s55, s46, s54
	s_cselect_b32 s54, s45, s53
	s_addk_i32 s21, 0x100
	s_and_b32 s53, s21, 0x780
	s_and_b64 s[30:31], s[34:35], exec
	s_cselect_b32 s30, s47, s53
	s_cselect_b32 s31, 0, 0
	s_add_u32 s30, s58, s30
	s_addc_u32 s31, s59, s31
	v_mov_b32_e32 v45, v1
	s_mov_b32 m0, s63
	s_add_u32 s53, s28, s53
	s_addc_u32 vcc_lo, s29, 0
	global_load_lds_dwordx4 v45, s[54:55]
	v_mov_b32_e32 v45, v190
	s_and_b64 s[34:35], s[34:35], exec
	s_mov_b32 m0, s64
	s_cselect_b32 s35, s49, vcc_lo
	s_cselect_b32 s34, s48, s53
	global_load_lds_dwordx4 v45, s[54:55]
	s_add_u32 s54, s54, 0x40000
	v_mov_b32_e32 v45, v1
	s_addc_u32 s55, s55, 0
	s_mov_b32 m0, s65
	s_nop 0
	global_load_lds_dwordx4 v45, s[54:55]
	v_mov_b32_e32 v45, v190
	s_mov_b32 m0, s66
	s_nop 0
	global_load_lds_dwordx4 v45, s[54:55]
	v_mov_b32_e32 v45, v192
	s_mov_b32 m0, s39
	s_nop 0
	global_load_lds_dwordx4 v45, s[36:37]
	v_mov_b32_e32 v45, v194
	s_mov_b32 m0, s67
	s_nop 0
	global_load_lds_dwordx4 v45, s[36:37]
	ds_read_b128 v[204:207], v200 offset:16384
	ds_read_b128 v[208:211], v200 offset:17408
	ds_read_b128 v[214:217], v200 offset:18432
	ds_read_b128 v[218:221], v200 offset:19456
	ds_read_b128 v[222:225], v200 offset:20480
	ds_read_b128 v[226:229], v200 offset:21504
	ds_read_b128 v[230:233], v200 offset:22528
	ds_read_b128 v[234:237], v200 offset:23552
	s_waitcnt vmcnt(8)
	s_waitcnt lgkmcnt(0)
	s_barrier
	s_setprio 1
	s_waitcnt lgkmcnt(0)
	s_nop 1
	v_mfma_scale_f32_16x16x128_f8f6f4 v[118:121], v[2:9], v[204:211], v[118:121], v191, v191 op_sel_hi:[0,0,0]
	v_mfma_scale_f32_16x16x128_f8f6f4 v[110:113], v[18:25], v[204:211], v[110:113], v191, v191 op_sel_hi:[0,0,0]
	v_mfma_scale_f32_16x16x128_f8f6f4 v[98:101], v[2:9], v[214:221], v[98:101], v191, v191 op_sel_hi:[0,0,0]
	v_mfma_scale_f32_16x16x128_f8f6f4 v[90:93], v[18:25], v[214:221], v[90:93], v191, v191 op_sel_hi:[0,0,0]
	v_mfma_scale_f32_16x16x128_f8f6f4 v[82:85], v[2:9], v[222:229], v[82:85], v191, v191 op_sel_hi:[0,0,0]
	v_mfma_scale_f32_16x16x128_f8f6f4 v[66:69], v[18:25], v[222:229], v[66:69], v191, v191 op_sel_hi:[0,0,0]
	v_mfma_scale_f32_16x16x128_f8f6f4 v[58:61], v[2:9], v[230:237], v[58:61], v191, v191 op_sel_hi:[0,0,0]
	v_mfma_scale_f32_16x16x128_f8f6f4 v[50:53], v[18:25], v[230:237], v[50:53], v191, v191 op_sel_hi:[0,0,0]
	s_setprio 0
	s_setprio 1
	s_nop 1
	v_mfma_scale_f32_16x16x128_f8f6f4 v[106:109], v[10:17], v[204:211], v[106:109], v191, v191 op_sel_hi:[0,0,0]
	v_mfma_scale_f32_16x16x128_f8f6f4 v[114:117], v[26:33], v[204:211], v[114:117], v191, v191 op_sel_hi:[0,0,0]
	v_mfma_scale_f32_16x16x128_f8f6f4 v[102:105], v[10:17], v[214:221], v[102:105], v191, v191 op_sel_hi:[0,0,0]
	v_mfma_scale_f32_16x16x128_f8f6f4 v[94:97], v[26:33], v[214:221], v[94:97], v191, v191 op_sel_hi:[0,0,0]
	v_mfma_scale_f32_16x16x128_f8f6f4 v[86:89], v[10:17], v[222:229], v[86:89], v191, v191 op_sel_hi:[0,0,0]
	v_mfma_scale_f32_16x16x128_f8f6f4 v[70:73], v[26:33], v[222:229], v[70:73], v191, v191 op_sel_hi:[0,0,0]
	v_mfma_scale_f32_16x16x128_f8f6f4 v[62:65], v[10:17], v[230:237], v[62:65], v191, v191 op_sel_hi:[0,0,0]
	v_mfma_scale_f32_16x16x128_f8f6f4 v[54:57], v[26:33], v[230:237], v[54:57], v191, v191 op_sel_hi:[0,0,0]
	s_setprio 0
	s_barrier
	ds_read_b128 v[2:5], v43
	ds_read_b128 v[6:9], v43 offset:1024
	ds_read_b128 v[10:13], v43 offset:2048
	ds_read_b128 v[14:17], v43 offset:3072
	ds_read_b128 v[18:21], v44
	ds_read_b128 v[22:25], v44 offset:1024
	ds_read_b128 v[26:29], v44 offset:2048
	ds_read_b128 v[30:33], v44 offset:3072
	v_mov_b32_e32 v45, v193
	s_mov_b32 m0, s68
	s_nop 0
	global_load_lds_dwordx4 v45, s[36:37]
	v_mov_b32_e32 v45, v195
	s_mov_b32 m0, s69
	s_nop 0
	global_load_lds_dwordx4 v45, s[36:37]
	ds_read_b128 v[204:207], v200 offset:32768
	ds_read_b128 v[208:211], v200 offset:33792
	ds_read_b128 v[214:217], v200 offset:34816
	ds_read_b128 v[218:221], v200 offset:35840
	ds_read_b128 v[222:225], v200 offset:36864
	ds_read_b128 v[226:229], v200 offset:37888
	ds_read_b128 v[230:233], v200 offset:38912
	ds_read_b128 v[234:237], v200 offset:39936
	s_waitcnt vmcnt(8)
	s_waitcnt lgkmcnt(0)
	s_barrier
	s_setprio 1
	s_waitcnt lgkmcnt(0)
	s_nop 1
	v_mfma_scale_f32_16x16x128_f8f6f4 v[178:181], v[2:9], v[204:211], v[178:181], v191, v191 op_sel_hi:[0,0,0]
	v_mfma_scale_f32_16x16x128_f8f6f4 v[170:173], v[10:17], v[204:211], v[170:173], v191, v191 op_sel_hi:[0,0,0]
	v_mfma_scale_f32_16x16x128_f8f6f4 v[162:165], v[2:9], v[214:221], v[162:165], v191, v191 op_sel_hi:[0,0,0]
	v_mfma_scale_f32_16x16x128_f8f6f4 v[154:157], v[10:17], v[214:221], v[154:157], v191, v191 op_sel_hi:[0,0,0]
	v_mfma_scale_f32_16x16x128_f8f6f4 v[146:149], v[2:9], v[222:229], v[146:149], v191, v191 op_sel_hi:[0,0,0]
	v_mfma_scale_f32_16x16x128_f8f6f4 v[138:141], v[10:17], v[222:229], v[138:141], v191, v191 op_sel_hi:[0,0,0]
	v_mfma_scale_f32_16x16x128_f8f6f4 v[130:133], v[2:9], v[230:237], v[130:133], v191, v191 op_sel_hi:[0,0,0]
	v_mfma_scale_f32_16x16x128_f8f6f4 v[122:125], v[10:17], v[230:237], v[122:125], v191, v191 op_sel_hi:[0,0,0]
	s_setprio 0
	s_setprio 1
	s_nop 1
	v_mfma_scale_f32_16x16x128_f8f6f4 v[182:185], v[18:25], v[204:211], v[182:185], v191, v191 op_sel_hi:[0,0,0]
	v_mfma_scale_f32_16x16x128_f8f6f4 v[174:177], v[26:33], v[204:211], v[174:177], v191, v191 op_sel_hi:[0,0,0]
	v_mfma_scale_f32_16x16x128_f8f6f4 v[166:169], v[18:25], v[214:221], v[166:169], v191, v191 op_sel_hi:[0,0,0]
	v_mfma_scale_f32_16x16x128_f8f6f4 v[158:161], v[26:33], v[214:221], v[158:161], v191, v191 op_sel_hi:[0,0,0]
	v_mfma_scale_f32_16x16x128_f8f6f4 v[150:153], v[18:25], v[222:229], v[150:153], v191, v191 op_sel_hi:[0,0,0]
	v_mfma_scale_f32_16x16x128_f8f6f4 v[142:145], v[26:33], v[222:229], v[142:145], v191, v191 op_sel_hi:[0,0,0]
	v_mfma_scale_f32_16x16x128_f8f6f4 v[134:137], v[18:25], v[230:237], v[134:137], v191, v191 op_sel_hi:[0,0,0]
	v_mfma_scale_f32_16x16x128_f8f6f4 v[126:129], v[26:33], v[230:237], v[126:129], v191, v191 op_sel_hi:[0,0,0]
	s_setprio 0
	s_barrier
; #define PG8_STAGE(bufoff, gbase, voff) do { if constexpr (!(Sched::CRIP & 2)) _Pragma("unroll") for (int _i = 0; _i < 2; ++_i) { unsigned _o = (voff)[_i]; asm volatile("" : "+v"(_o)); \
;         __builtin_amdgcn_global_load_lds((const unsigned*)((const char*)(gbase) + _o), (LAS unsigned*)(lds + (bufoff) + ldsw + _i * 8192), 16, 0, 0); } } while (0)
; #define PG8_LDA(dst, b, h) do { if constexpr (!(Sched::CRIP & 4)) _Pragma("unroll") for (int m = 0; m < 4; ++m) dst[m] = PG8_CAT(*(const LAS i32x4*)(lds + PG8_SA(b, h) + aoff + m * 2048), *(const LAS i32x4*)(lds + PG8_SA(b, h) + aoff + m * 2048 + 1024)); } while (0)
; #define PG8_LDB(dst, b, h) do { if constexpr (!(Sched::CRIP & 4)) _Pragma("unroll") for (int n = 0; n < 2; ++n) dst[n] = PG8_CAT(*(const LAS i32x4*)(lds + PG8_SB(b, h) + boff + n * 2048), *(const LAS i32x4*)(lds + PG8_SB(b, h) + boff + n * 2048 + 1024)); } while (0)
; #define PG8_WAIT_V(n) asm volatile("s_waitcnt vmcnt(" #n ")" ::: "memory")
; #define PG8_WAIT_L(n) asm volatile("s_waitcnt lgkmcnt(" #n ")" ::: "memory")
; #define PG8_BAR __builtin_amdgcn_s_barrier()
; #define PG8_SCHED __builtin_amdgcn_sched_barrier(0)
; template <class Epi, class Sched>
; __device__ __forceinline__ void gemm_phase(LAS unsigned char* lds, const Sched& S, const Epi& E) {
;     ...
;             PG8_LDB(B0, 0, 0); PG8_LDB(B1, 0, 1); PG8_SCHED; PG8_LDA(At, 0, 0); PG8_STAGE(PG8_SA(1, 1), a1, vA[1]);
;             PG8_WAIT_V(8); PG8_WAIT_L(0); PG8_BAR; PG8_MMA(0, 0, At, B0); PG8_MMA(0, 1, At, B1); PG8_BAR2; PG8_SCHED;
;             if constexpr (Sched::GATHER) { if (last && has_next) {
;                 int tz = threadIdx.x; asm volatile("" : "+v"(tz));
; #pragma unroll
;                 for (int i = 0; i < 2; ++i) { int R, C; stage_rc(tz * 16 + i * 8192, R, C);
; #pragma unroll
;                     for (int h = 0; h < 2; ++h) vA[h][i] = (unsigned)(lidx[h * HALF + R] * RP + C * 2); } } }
;     ...
;             PG8_LDA(At, 1, 1); PG8_STAGE(PG8_SB(1, 0), b3, voffB); PG8_STAGE(PG8_SB(1, 1), b3 + hstep, voffB); PG8_STAGE(PG8_SA(1, 0), a3, vA[0]);
;             PG8_WAIT_V(8); PG8_WAIT_L(0); PG8_BAR; PG8_MMA(1, 0, At, B0); PG8_MMA(1, 1, At, B1); PG8_BAR2; PG8_SCHED;
	v_mov_b32_e32 v45, v1
	s_mov_b32 m0, s40
	s_nop 0
	global_load_lds_dwordx4 v45, s[34:35]
	v_mov_b32_e32 v45, v190
	s_mov_b32 m0, s41
	s_nop 0
	global_load_lds_dwordx4 v45, s[34:35]
	s_add_u32 s34, s34, 0x40000
	v_mov_b32_e32 v45, v1
	s_addc_u32 s35, s35, 0
	s_mov_b32 m0, s42
	s_nop 0
	global_load_lds_dwordx4 v45, s[34:35]
	v_mov_b32_e32 v45, v190
	s_mov_b32 m0, s43
	s_nop 0
	global_load_lds_dwordx4 v45, s[34:35]
	v_mov_b32_e32 v45, v192
	s_mov_b32 m0, s70
	s_nop 0
	global_load_lds_dwordx4 v45, s[30:31]
	v_mov_b32_e32 v45, v194
	s_mov_b32 m0, s71
	s_nop 0
	global_load_lds_dwordx4 v45, s[30:31]
	ds_read_b128 v[204:207], v200 offset:49152
	ds_read_b128 v[208:211], v200 offset:50176
	ds_read_b128 v[214:217], v200 offset:51200
	ds_read_b128 v[218:221], v200 offset:52224
	ds_read_b128 v[222:225], v200 offset:53248
	ds_read_b128 v[226:229], v200 offset:54272
	ds_read_b128 v[230:233], v200 offset:55296
	ds_read_b128 v[234:237], v200 offset:56320
	s_waitcnt vmcnt(8)
	s_waitcnt lgkmcnt(0)
	s_barrier
	s_setprio 1
	s_waitcnt lgkmcnt(0)
	s_nop 1
	v_mfma_scale_f32_16x16x128_f8f6f4 v[118:121], v[2:9], v[204:211], v[118:121], v191, v191 op_sel_hi:[0,0,0]
	v_mfma_scale_f32_16x16x128_f8f6f4 v[110:113], v[10:17], v[204:211], v[110:113], v191, v191 op_sel_hi:[0,0,0]
	v_mfma_scale_f32_16x16x128_f8f6f4 v[98:101], v[2:9], v[214:221], v[98:101], v191, v191 op_sel_hi:[0,0,0]
	v_mfma_scale_f32_16x16x128_f8f6f4 v[90:93], v[10:17], v[214:221], v[90:93], v191, v191 op_sel_hi:[0,0,0]
	v_mfma_scale_f32_16x16x128_f8f6f4 v[82:85], v[2:9], v[222:229], v[82:85], v191, v191 op_sel_hi:[0,0,0]
	v_mfma_scale_f32_16x16x128_f8f6f4 v[66:69], v[10:17], v[222:229], v[66:69], v191, v191 op_sel_hi:[0,0,0]
	v_mfma_scale_f32_16x16x128_f8f6f4 v[58:61], v[2:9], v[230:237], v[58:61], v191, v191 op_sel_hi:[0,0,0]
	v_mfma_scale_f32_16x16x128_f8f6f4 v[50:53], v[10:17], v[230:237], v[50:53], v191, v191 op_sel_hi:[0,0,0]
	s_setprio 0
	s_setprio 1
	s_nop 1
	v_mfma_scale_f32_16x16x128_f8f6f4 v[106:109], v[18:25], v[204:211], v[106:109], v191, v191 op_sel_hi:[0,0,0]
	v_mfma_scale_f32_16x16x128_f8f6f4 v[114:117], v[26:33], v[204:211], v[114:117], v191, v191 op_sel_hi:[0,0,0]
	v_mfma_scale_f32_16x16x128_f8f6f4 v[102:105], v[18:25], v[214:221], v[102:105], v191, v191 op_sel_hi:[0,0,0]
	v_mfma_scale_f32_16x16x128_f8f6f4 v[94:97], v[26:33], v[214:221], v[94:97], v191, v191 op_sel_hi:[0,0,0]
	v_mfma_scale_f32_16x16x128_f8f6f4 v[86:89], v[18:25], v[222:229], v[86:89], v191, v191 op_sel_hi:[0,0,0]
	v_mfma_scale_f32_16x16x128_f8f6f4 v[70:73], v[26:33], v[222:229], v[70:73], v191, v191 op_sel_hi:[0,0,0]
	v_mfma_scale_f32_16x16x128_f8f6f4 v[62:65], v[18:25], v[230:237], v[62:65], v191, v191 op_sel_hi:[0,0,0]
	v_mfma_scale_f32_16x16x128_f8f6f4 v[54:57], v[26:33], v[230:237], v[54:57], v191, v191 op_sel_hi:[0,0,0]
	s_setprio 0
	s_barrier
	s_add_i32 s52, s52, 2
	s_cmp_gt_u32 s52, 13
	s_cbranch_scc1 .LBB0_737
.LBB0_735:
	v_add_u32_e32 v10, 0, v196
	v_add_u32_e32 v11, 0x10000, v10
	v_add_u32_e32 v30, 0x14000, v10
	ds_read_b128 v[2:5], v11
	ds_read_b128 v[6:9], v11 offset:1024
	ds_read_b128 v[18:21], v11 offset:2048
	ds_read_b128 v[22:25], v11 offset:3072
	ds_read_b128 v[10:13], v30
	ds_read_b128 v[14:17], v30 offset:1024
	ds_read_b128 v[26:29], v30 offset:2048
	ds_read_b128 v[30:33], v30 offset:3072
	s_cmp_eq_u32 s52, 12
	s_cselect_b64 s[34:35], -1, 0
	s_and_b32 s30, s21, 0x780
	s_add_u32 s30, s58, s30
	s_addc_u32 s31, s59, 0
	v_mov_b32_e32 v45, v193
	s_mov_b32 m0, s27
	s_nop 0
	global_load_lds_dwordx4 v45, s[30:31]
	v_mov_b32_e32 v45, v195
	s_mov_b32 m0, s62
	s_nop 0
	global_load_lds_dwordx4 v45, s[30:31]
	ds_read_b128 v[204:207], v200
	ds_read_b128 v[208:211], v200 offset:1024
	ds_read_b128 v[214:217], v200 offset:2048
	ds_read_b128 v[218:221], v200 offset:3072
	ds_read_b128 v[222:225], v200 offset:4096
	ds_read_b128 v[226:229], v200 offset:5120
	ds_read_b128 v[230:233], v200 offset:6144
	ds_read_b128 v[234:237], v200 offset:7168
	s_waitcnt vmcnt(8)
	s_waitcnt lgkmcnt(0)
	s_barrier
	s_setprio 1
	s_waitcnt lgkmcnt(0)
	s_nop 1
	v_mfma_scale_f32_16x16x128_f8f6f4 v[178:181], v[2:9], v[204:211], v[178:181], v191, v191 op_sel_hi:[0,0,0]
	v_mfma_scale_f32_16x16x128_f8f6f4 v[170:173], v[18:25], v[204:211], v[170:173], v191, v191 op_sel_hi:[0,0,0]
	v_mfma_scale_f32_16x16x128_f8f6f4 v[162:165], v[2:9], v[214:221], v[162:165], v191, v191 op_sel_hi:[0,0,0]
	v_mfma_scale_f32_16x16x128_f8f6f4 v[154:157], v[18:25], v[214:221], v[154:157], v191, v191 op_sel_hi:[0,0,0]
	v_mfma_scale_f32_16x16x128_f8f6f4 v[146:149], v[2:9], v[222:229], v[146:149], v191, v191 op_sel_hi:[0,0,0]
	v_mfma_scale_f32_16x16x128_f8f6f4 v[138:141], v[18:25], v[222:229], v[138:141], v191, v191 op_sel_hi:[0,0,0]
	v_mfma_scale_f32_16x16x128_f8f6f4 v[130:133], v[2:9], v[230:237], v[130:133], v191, v191 op_sel_hi:[0,0,0]
	v_mfma_scale_f32_16x16x128_f8f6f4 v[122:125], v[18:25], v[230:237], v[122:125], v191, v191 op_sel_hi:[0,0,0]
	s_setprio 0
	s_setprio 1
	s_nop 1
	v_mfma_scale_f32_16x16x128_f8f6f4 v[182:185], v[10:17], v[204:211], v[182:185], v191, v191 op_sel_hi:[0,0,0]
	v_mfma_scale_f32_16x16x128_f8f6f4 v[174:177], v[26:33], v[204:211], v[174:177], v191, v191 op_sel_hi:[0,0,0]
	v_mfma_scale_f32_16x16x128_f8f6f4 v[166:169], v[10:17], v[214:221], v[166:169], v191, v191 op_sel_hi:[0,0,0]
	v_mfma_scale_f32_16x16x128_f8f6f4 v[158:161], v[26:33], v[214:221], v[158:161], v191, v191 op_sel_hi:[0,0,0]
	v_mfma_scale_f32_16x16x128_f8f6f4 v[150:153], v[10:17], v[222:229], v[150:153], v191, v191 op_sel_hi:[0,0,0]
	v_mfma_scale_f32_16x16x128_f8f6f4 v[142:145], v[26:33], v[222:229], v[142:145], v191, v191 op_sel_hi:[0,0,0]
	v_mfma_scale_f32_16x16x128_f8f6f4 v[134:137], v[10:17], v[230:237], v[134:137], v191, v191 op_sel_hi:[0,0,0]
	v_mfma_scale_f32_16x16x128_f8f6f4 v[126:129], v[26:33], v[230:237], v[126:129], v191, v191 op_sel_hi:[0,0,0]
	s_setprio 0
	s_barrier
	s_and_b64 s[30:31], s[2:3], s[34:35]
	s_andn2_b64 vcc, exec, s[30:31]
	s_cbranch_vccnz .LBB0_734
	ds_read2st64_b32 v[48:49], v246 offset1:2
	ds_read2st64_b32 v[250:251], v248 offset1:2
	s_waitcnt lgkmcnt(0)
	v_lshl_add_u32 v192, v48, 11, v247
	v_lshl_add_u32 v193, v49, 11, v247
	v_lshl_add_u32 v194, v250, 11, v249
	v_lshl_add_u32 v195, v251, 11, v249
	s_branch .LBB0_734

; #define PG8_STAGE(bufoff, gbase, voff) do { if constexpr (!(Sched::CRIP & 2)) _Pragma("unroll") for (int _i = 0; _i < 2; ++_i) { unsigned _o = (voff)[_i]; asm volatile("" : "+v"(_o)); \
;         __builtin_amdgcn_global_load_lds((const unsigned*)((const char*)(gbase) + _o), (LAS unsigned*)(lds + (bufoff) + ldsw + _i * 8192), 16, 0, 0); } } while (0)
; #define PG8_LDA(dst, b, h) do { if constexpr (!(Sched::CRIP & 4)) _Pragma("unroll") for (int m = 0; m < 4; ++m) dst[m] = PG8_CAT(*(const LAS i32x4*)(lds + PG8_SA(b, h) + aoff + m * 2048), *(const LAS i32x4*)(lds + PG8_SA(b, h) + aoff + m * 2048 + 1024)); } while (0)
; #define PG8_LDB(dst, b, h) do { if constexpr (!(Sched::CRIP & 4)) _Pragma("unroll") for (int n = 0; n < 2; ++n) dst[n] = PG8_CAT(*(const LAS i32x4*)(lds + PG8_SB(b, h) + boff + n * 2048), *(const LAS i32x4*)(lds + PG8_SB(b, h) + boff + n * 2048 + 1024)); } while (0)
; #define PG8_WAIT_V(n) asm volatile("s_waitcnt vmcnt(" #n ")" ::: "memory")
; #define PG8_WAIT_L(n) asm volatile("s_waitcnt lgkmcnt(" #n ")" ::: "memory")
; #define PG8_BAR __builtin_amdgcn_s_barrier()
; #define PG8_SCHED __builtin_amdgcn_sched_barrier(0)
; template <class Epi, class Sched>
; __device__ __forceinline__ void gemm_phase(LAS unsigned char* lds, const Sched& S, const Epi& E) {
;     ...
;             PG8_LDB(B0, 0, 0); PG8_LDB(B1, 0, 1); PG8_SCHED; PG8_LDA(At, 0, 0); PG8_STAGE(PG8_SA(1, 1), a1, vA[1]);
;             PG8_WAIT_V(8); PG8_WAIT_L(0); PG8_BAR; PG8_MMA(0, 0, At, B0); PG8_MMA(0, 1, At, B1); PG8_BAR2; PG8_SCHED;
;             if constexpr (Sched::GATHER) { if (last && has_next) {
;                 int tz = threadIdx.x; asm volatile("" : "+v"(tz));
; #pragma unroll
;                 for (int i = 0; i < 2; ++i) { int R, C; stage_rc(tz * 16 + i * 8192, R, C);
; #pragma unroll
;                     for (int h = 0; h < 2; ++h) vA[h][i] = (unsigned)(lidx[h * HALF + R] * RP + C * 2); } } }
;             PG8_LDA(At, 0, 1); PG8_STAGE(PG8_SB(0, 0), b2, voffB); PG8_STAGE(PG8_SB(0, 1), b2 + hstep, voffB); PG8_STAGE(PG8_SA(0, 0), a2, vA[0]);
;             PG8_WAIT_V(8); PG8_WAIT_L(0); PG8_BAR; PG8_MMA(1, 0, At, B0); PG8_MMA(1, 1, At, B1); PG8_BAR2; PG8_SCHED;
.LBB0_806:
	s_and_b32 s13, s12, 15
	s_and_b64 s[30:31], s[0:1], exec
	s_cselect_b32 s15, s13, s34
	s_lshl_b32 s30, s15, 7
	s_add_u32 s15, s92, s30
	s_addc_u32 s17, s93, 0
	s_add_u32 s25, s94, s30
	s_addc_u32 s38, s95, 0
	s_addk_i32 s30, 0x80
	s_and_b32 s30, s30, 0x780
	s_add_u32 s39, s92, s30
	s_addc_u32 s80, s93, 0
	s_add_u32 s81, s94, s30
	s_addc_u32 s82, s95, 0
	s_lshl_b32 s30, s34, 7
	s_add_i32 s83, s30, 0x180
	s_mov_b32 s84, -2
	s_add_i32 s30, s83, 0xffffff00
	s_add_i32 s31, s83, 0xffffff80
	s_and_b32 s30, s30, 0x780
	s_and_b32 s31, s31, 0x780
	s_add_u32 s34, s26, s31
	s_addc_u32 s35, s27, 0
	s_add_u32 s40, s28, s31
	s_addc_u32 s41, s29, 0
	s_and_b32 s31, s83, 0x780
	s_add_u32 s53, s26, s31
	v_add_u32_e32 v2, s77, v186
	v_add_u32_e32 v22, s78, v186
	s_addc_u32 s85, s27, 0
	ds_read_b128 v[10:13], v2
	ds_read_b128 v[14:17], v2 offset:1024
	ds_read_b128 v[26:29], v2 offset:2048
	ds_read_b128 v[30:33], v2 offset:3072
	ds_read_b128 v[2:5], v22
	ds_read_b128 v[6:9], v22 offset:1024
	ds_read_b128 v[18:21], v22 offset:2048
	ds_read_b128 v[22:25], v22 offset:3072
	s_add_u32 s36, s28, s31
	s_addc_u32 s37, s29, 0
	s_add_u32 s54, s26, s30
	s_addc_u32 s55, s27, 0
	s_add_i32 s87, s77, s47
	s_add_i32 m0, s69, 0xc000
	s_add_i32 s86, s69, 0xe000
	s_add_i32 s52, s87, 0x2000
	s_cmp_eq_u32 s84, 12
	s_cselect_b32 s35, s17, s35
	s_cselect_b32 s34, s15, s34
	s_cselect_b32 s31, s80, s85
	s_cselect_b32 s30, s39, s53
	s_cselect_b32 s41, s38, s41
	s_cselect_b32 s40, s25, s40
	v_mov_b32_e32 v178, v183
	s_nop 0
	global_load_lds_dwordx4 v178, s[54:55]
	v_mov_b32_e32 v178, v184
	s_mov_b32 m0, s86
	s_nop 0
	global_load_lds_dwordx4 v178, s[54:55]
	ds_read_b128 v[198:201], v188
	ds_read_b128 v[202:205], v188 offset:1024
	ds_read_b128 v[214:217], v188 offset:2048
	ds_read_b128 v[218:221], v188 offset:3072
	ds_read_b128 v[222:225], v188 offset:4096
	ds_read_b128 v[226:229], v188 offset:5120
	ds_read_b128 v[230:233], v188 offset:6144
	ds_read_b128 v[234:237], v188 offset:7168
	s_waitcnt vmcnt(28)
	s_waitcnt lgkmcnt(0)
	s_barrier
	s_setprio 1
	s_waitcnt lgkmcnt(0)
	s_nop 1
	v_mfma_scale_f32_16x16x128_f8f6f4 v[174:177], v[10:17], v[198:205], 0, v185, v185 op_sel_hi:[0,0,0]
	v_mfma_scale_f32_16x16x128_f8f6f4 v[170:173], v[26:33], v[198:205], 0, v185, v185 op_sel_hi:[0,0,0]
	v_mfma_scale_f32_16x16x128_f8f6f4 v[166:169], v[10:17], v[214:221], 0, v185, v185 op_sel_hi:[0,0,0]
	v_mfma_scale_f32_16x16x128_f8f6f4 v[162:165], v[26:33], v[214:221], 0, v185, v185 op_sel_hi:[0,0,0]
	v_mfma_scale_f32_16x16x128_f8f6f4 v[142:145], v[10:17], v[222:229], 0, v185, v185 op_sel_hi:[0,0,0]
	v_mfma_scale_f32_16x16x128_f8f6f4 v[138:141], v[26:33], v[222:229], 0, v185, v185 op_sel_hi:[0,0,0]
	v_mfma_scale_f32_16x16x128_f8f6f4 v[134:137], v[10:17], v[230:237], 0, v185, v185 op_sel_hi:[0,0,0]
	v_mfma_scale_f32_16x16x128_f8f6f4 v[130:133], v[26:33], v[230:237], 0, v185, v185 op_sel_hi:[0,0,0]
	s_setprio 0
	s_setprio 1
	s_nop 1
	v_mfma_scale_f32_16x16x128_f8f6f4 v[158:161], v[2:9], v[198:205], 0, v185, v185 op_sel_hi:[0,0,0]
	v_mfma_scale_f32_16x16x128_f8f6f4 v[154:157], v[18:25], v[198:205], 0, v185, v185 op_sel_hi:[0,0,0]
	v_mfma_scale_f32_16x16x128_f8f6f4 v[150:153], v[2:9], v[214:221], 0, v185, v185 op_sel_hi:[0,0,0]
	v_mfma_scale_f32_16x16x128_f8f6f4 v[146:149], v[18:25], v[214:221], 0, v185, v185 op_sel_hi:[0,0,0]
	v_mfma_scale_f32_16x16x128_f8f6f4 v[126:129], v[2:9], v[222:229], 0, v185, v185 op_sel_hi:[0,0,0]
	v_mfma_scale_f32_16x16x128_f8f6f4 v[122:125], v[18:25], v[222:229], 0, v185, v185 op_sel_hi:[0,0,0]
	v_mfma_scale_f32_16x16x128_f8f6f4 v[118:121], v[2:9], v[230:237], 0, v185, v185 op_sel_hi:[0,0,0]
	v_mfma_scale_f32_16x16x128_f8f6f4 v[114:117], v[18:25], v[230:237], 0, v185, v185 op_sel_hi:[0,0,0]
	s_setprio 0
	s_barrier
	v_mov_b32_e32 v178, v1
	s_mov_b32 m0, s87
	s_cselect_b32 s36, s81, s36
	global_load_lds_dwordx4 v178, s[40:41]
	v_mov_b32_e32 v178, v180
	s_mov_b32 m0, s52
	s_cselect_b32 s37, s82, s37
	global_load_lds_dwordx4 v178, s[40:41]
	s_add_u32 s40, s40, 0x40000
	v_mov_b32_e32 v178, v1
	s_addc_u32 s41, s41, 0
	s_add_i32 s52, s78, s47
	s_mov_b32 m0, s52
	s_nop 0
	global_load_lds_dwordx4 v178, s[40:41]
	v_mov_b32_e32 v178, v180
	s_add_i32 m0, s52, 0x2000
	s_nop 0
	global_load_lds_dwordx4 v178, s[40:41]
	v_mov_b32_e32 v178, v181
	s_mov_b32 m0, s69
	s_nop 0
	global_load_lds_dwordx4 v178, s[34:35]
	v_mov_b32_e32 v178, v182
	s_mov_b32 m0, s70
	s_nop 0
	global_load_lds_dwordx4 v178, s[34:35]
	ds_read_b128 v[198:201], v188 offset:16384
	ds_read_b128 v[202:205], v188 offset:17408
	ds_read_b128 v[214:217], v188 offset:18432
	ds_read_b128 v[218:221], v188 offset:19456
	ds_read_b128 v[222:225], v188 offset:20480
	ds_read_b128 v[226:229], v188 offset:21504
	ds_read_b128 v[230:233], v188 offset:22528
	ds_read_b128 v[234:237], v188 offset:23552
	s_waitcnt vmcnt(28)
	s_waitcnt lgkmcnt(0)
	s_barrier
; #define PG8_STAGE(bufoff, gbase, voff) do { if constexpr (!(Sched::CRIP & 2)) _Pragma("unroll") for (int _i = 0; _i < 2; ++_i) { unsigned _o = (voff)[_i]; asm volatile("" : "+v"(_o)); \
;         __builtin_amdgcn_global_load_lds((const unsigned*)((const char*)(gbase) + _o), (LAS unsigned*)(lds + (bufoff) + ldsw + _i * 8192), 16, 0, 0); } } while (0)
; #define PG8_LDA(dst, b, h) do { if constexpr (!(Sched::CRIP & 4)) _Pragma("unroll") for (int m = 0; m < 4; ++m) dst[m] = PG8_CAT(*(const LAS i32x4*)(lds + PG8_SA(b, h) + aoff + m * 2048), *(const LAS i32x4*)(lds + PG8_SA(b, h) + aoff + m * 2048 + 1024)); } while (0)
; #define PG8_LDB(dst, b, h) do { if constexpr (!(Sched::CRIP & 4)) _Pragma("unroll") for (int n = 0; n < 2; ++n) dst[n] = PG8_CAT(*(const LAS i32x4*)(lds + PG8_SB(b, h) + boff + n * 2048), *(const LAS i32x4*)(lds + PG8_SB(b, h) + boff + n * 2048 + 1024)); } while (0)
; #define PG8_WAIT_V(n) asm volatile("s_waitcnt vmcnt(" #n ")" ::: "memory")
; #define PG8_WAIT_L(n) asm volatile("s_waitcnt lgkmcnt(" #n ")" ::: "memory")
; #define PG8_BAR __builtin_amdgcn_s_barrier()
; #define PG8_SCHED __builtin_amdgcn_sched_barrier(0)
; template <class Epi, class Sched>
; __device__ __forceinline__ void gemm_phase(LAS unsigned char* lds, const Sched& S, const Epi& E) {
;     ...
;             PG8_WAIT_V(8); PG8_WAIT_L(0); PG8_BAR; PG8_MMA(1, 0, At, B0); PG8_MMA(1, 1, At, B1); PG8_BAR2; PG8_SCHED;
;             PG8_LDB(B0, 1, 0); PG8_LDB(B1, 1, 1); PG8_SCHED; PG8_LDA(At, 1, 0); PG8_STAGE(PG8_SA(0, 1), a2, vA[1]);
;             PG8_WAIT_V(8); PG8_WAIT_L(0); PG8_BAR; PG8_MMA(0, 0, At, B0); PG8_MMA(0, 1, At, B1); PG8_BAR2; PG8_SCHED;
;             PG8_LDA(At, 1, 1); PG8_STAGE(PG8_SB(1, 0), b3, voffB); PG8_STAGE(PG8_SB(1, 1), b3 + hstep, voffB); PG8_STAGE(PG8_SA(1, 0), a3, vA[0]);
;             PG8_WAIT_V(8); PG8_WAIT_L(0); PG8_BAR; PG8_MMA(1, 0, At, B0); PG8_MMA(1, 1, At, B1); PG8_BAR2; PG8_SCHED;
	s_setprio 1
	s_waitcnt lgkmcnt(0)
	s_nop 1
	v_mfma_scale_f32_16x16x128_f8f6f4 v[110:113], v[10:17], v[198:205], 0, v185, v185 op_sel_hi:[0,0,0]
	v_mfma_scale_f32_16x16x128_f8f6f4 v[106:109], v[26:33], v[198:205], 0, v185, v185 op_sel_hi:[0,0,0]
	v_mfma_scale_f32_16x16x128_f8f6f4 v[102:105], v[10:17], v[214:221], 0, v185, v185 op_sel_hi:[0,0,0]
	v_mfma_scale_f32_16x16x128_f8f6f4 v[98:101], v[26:33], v[214:221], 0, v185, v185 op_sel_hi:[0,0,0]
	v_mfma_scale_f32_16x16x128_f8f6f4 v[78:81], v[10:17], v[222:229], 0, v185, v185 op_sel_hi:[0,0,0]
	v_mfma_scale_f32_16x16x128_f8f6f4 v[74:77], v[26:33], v[222:229], 0, v185, v185 op_sel_hi:[0,0,0]
	v_mfma_scale_f32_16x16x128_f8f6f4 v[70:73], v[10:17], v[230:237], 0, v185, v185 op_sel_hi:[0,0,0]
	v_mfma_scale_f32_16x16x128_f8f6f4 v[66:69], v[26:33], v[230:237], 0, v185, v185 op_sel_hi:[0,0,0]
	s_setprio 0
	s_setprio 1
	s_nop 1
	v_mfma_scale_f32_16x16x128_f8f6f4 v[94:97], v[2:9], v[198:205], 0, v185, v185 op_sel_hi:[0,0,0]
	v_mfma_scale_f32_16x16x128_f8f6f4 v[90:93], v[18:25], v[198:205], 0, v185, v185 op_sel_hi:[0,0,0]
	v_mfma_scale_f32_16x16x128_f8f6f4 v[86:89], v[2:9], v[214:221], 0, v185, v185 op_sel_hi:[0,0,0]
	v_mfma_scale_f32_16x16x128_f8f6f4 v[82:85], v[18:25], v[214:221], 0, v185, v185 op_sel_hi:[0,0,0]
	v_mfma_scale_f32_16x16x128_f8f6f4 v[62:65], v[2:9], v[222:229], 0, v185, v185 op_sel_hi:[0,0,0]
	v_mfma_scale_f32_16x16x128_f8f6f4 v[58:61], v[18:25], v[222:229], 0, v185, v185 op_sel_hi:[0,0,0]
	v_mfma_scale_f32_16x16x128_f8f6f4 v[54:57], v[2:9], v[230:237], 0, v185, v185 op_sel_hi:[0,0,0]
	v_mfma_scale_f32_16x16x128_f8f6f4 v[50:53], v[18:25], v[230:237], 0, v185, v185 op_sel_hi:[0,0,0]
	s_setprio 0
	s_barrier
	s_add_i32 s40, 0, 0x18000
	s_add_i32 s41, 0, 0x1c000
	v_add_u32_e32 v14, s40, v186
	v_add_u32_e32 v30, s41, v186
	ds_read_b128 v[2:5], v14
	ds_read_b128 v[6:9], v14 offset:1024
	ds_read_b128 v[10:13], v14 offset:2048
	ds_read_b128 v[14:17], v14 offset:3072
	ds_read_b128 v[18:21], v30
	ds_read_b128 v[22:25], v30 offset:1024
	ds_read_b128 v[26:29], v30 offset:2048
	ds_read_b128 v[30:33], v30 offset:3072
	v_mov_b32_e32 v178, v183
	s_mov_b32 m0, s71
	s_nop 0
	global_load_lds_dwordx4 v178, s[34:35]
	v_mov_b32_e32 v178, v184
	s_mov_b32 m0, s72
	s_nop 0
	global_load_lds_dwordx4 v178, s[34:35]
	ds_read_b128 v[198:201], v188 offset:32768
	ds_read_b128 v[202:205], v188 offset:33792
	ds_read_b128 v[214:217], v188 offset:34816
	ds_read_b128 v[218:221], v188 offset:35840
	ds_read_b128 v[222:225], v188 offset:36864
	ds_read_b128 v[226:229], v188 offset:37888
	ds_read_b128 v[230:233], v188 offset:38912
	ds_read_b128 v[234:237], v188 offset:39936
	s_waitcnt vmcnt(8)
	s_waitcnt lgkmcnt(0)
	s_barrier
	s_setprio 1
	s_waitcnt lgkmcnt(0)
	s_nop 1
	v_mfma_scale_f32_16x16x128_f8f6f4 v[174:177], v[2:9], v[198:205], v[174:177], v185, v185 op_sel_hi:[0,0,0]
	v_mfma_scale_f32_16x16x128_f8f6f4 v[170:173], v[10:17], v[198:205], v[170:173], v185, v185 op_sel_hi:[0,0,0]
	v_mfma_scale_f32_16x16x128_f8f6f4 v[166:169], v[2:9], v[214:221], v[166:169], v185, v185 op_sel_hi:[0,0,0]
	v_mfma_scale_f32_16x16x128_f8f6f4 v[162:165], v[10:17], v[214:221], v[162:165], v185, v185 op_sel_hi:[0,0,0]
	v_mfma_scale_f32_16x16x128_f8f6f4 v[142:145], v[2:9], v[222:229], v[142:145], v185, v185 op_sel_hi:[0,0,0]
	v_mfma_scale_f32_16x16x128_f8f6f4 v[138:141], v[10:17], v[222:229], v[138:141], v185, v185 op_sel_hi:[0,0,0]
	v_mfma_scale_f32_16x16x128_f8f6f4 v[134:137], v[2:9], v[230:237], v[134:137], v185, v185 op_sel_hi:[0,0,0]
	v_mfma_scale_f32_16x16x128_f8f6f4 v[130:133], v[10:17], v[230:237], v[130:133], v185, v185 op_sel_hi:[0,0,0]
	s_setprio 0
	s_setprio 1
	s_nop 1
	v_mfma_scale_f32_16x16x128_f8f6f4 v[158:161], v[18:25], v[198:205], v[158:161], v185, v185 op_sel_hi:[0,0,0]
	v_mfma_scale_f32_16x16x128_f8f6f4 v[154:157], v[26:33], v[198:205], v[154:157], v185, v185 op_sel_hi:[0,0,0]
	v_mfma_scale_f32_16x16x128_f8f6f4 v[150:153], v[18:25], v[214:221], v[150:153], v185, v185 op_sel_hi:[0,0,0]
	v_mfma_scale_f32_16x16x128_f8f6f4 v[146:149], v[26:33], v[214:221], v[146:149], v185, v185 op_sel_hi:[0,0,0]
	v_mfma_scale_f32_16x16x128_f8f6f4 v[126:129], v[18:25], v[222:229], v[126:129], v185, v185 op_sel_hi:[0,0,0]
	v_mfma_scale_f32_16x16x128_f8f6f4 v[122:125], v[26:33], v[222:229], v[122:125], v185, v185 op_sel_hi:[0,0,0]
	v_mfma_scale_f32_16x16x128_f8f6f4 v[118:121], v[18:25], v[230:237], v[118:121], v185, v185 op_sel_hi:[0,0,0]
	v_mfma_scale_f32_16x16x128_f8f6f4 v[114:117], v[26:33], v[230:237], v[114:117], v185, v185 op_sel_hi:[0,0,0]
	s_setprio 0
	s_barrier
	v_mov_b32_e32 v178, v1
	s_add_i32 s34, s40, s47
	s_mov_b32 m0, s34
	s_nop 0
	global_load_lds_dwordx4 v178, s[36:37]
	v_mov_b32_e32 v178, v180
	s_add_i32 m0, s34, 0x2000
	s_add_u32 s34, s36, 0x40000
	global_load_lds_dwordx4 v178, s[36:37]
	s_addc_u32 s35, s37, 0
	v_mov_b32_e32 v178, v1
	s_add_i32 s36, s41, s47
	s_mov_b32 m0, s36
	s_nop 0
	global_load_lds_dwordx4 v178, s[34:35]
	v_mov_b32_e32 v178, v180
	s_add_i32 m0, s36, 0x2000
	s_nop 0
	global_load_lds_dwordx4 v178, s[34:35]
	v_mov_b32_e32 v178, v181
	s_mov_b32 m0, s74
	s_nop 0
	global_load_lds_dwordx4 v178, s[30:31]
	v_mov_b32_e32 v178, v182
	s_mov_b32 m0, s75
	s_nop 0
	global_load_lds_dwordx4 v178, s[30:31]
	ds_read_b128 v[198:201], v188 offset:49152
	ds_read_b128 v[202:205], v188 offset:50176
	ds_read_b128 v[214:217], v188 offset:51200
	ds_read_b128 v[218:221], v188 offset:52224
	ds_read_b128 v[222:225], v188 offset:53248
	ds_read_b128 v[226:229], v188 offset:54272
	ds_read_b128 v[230:233], v188 offset:55296
	ds_read_b128 v[234:237], v188 offset:56320
	s_waitcnt vmcnt(8)
	s_waitcnt lgkmcnt(0)
	s_barrier
; #define PG8_STAGE(bufoff, gbase, voff) do { if constexpr (!(Sched::CRIP & 2)) _Pragma("unroll") for (int _i = 0; _i < 2; ++_i) { unsigned _o = (voff)[_i]; asm volatile("" : "+v"(_o)); \
;         __builtin_amdgcn_global_load_lds((const unsigned*)((const char*)(gbase) + _o), (LAS unsigned*)(lds + (bufoff) + ldsw + _i * 8192), 16, 0, 0); } } while (0)
; #define PG8_LDA(dst, b, h) do { if constexpr (!(Sched::CRIP & 4)) _Pragma("unroll") for (int m = 0; m < 4; ++m) dst[m] = PG8_CAT(*(const LAS i32x4*)(lds + PG8_SA(b, h) + aoff + m * 2048), *(const LAS i32x4*)(lds + PG8_SA(b, h) + aoff + m * 2048 + 1024)); } while (0)
; #define PG8_WAIT_V(n) asm volatile("s_waitcnt vmcnt(" #n ")" ::: "memory")
; #define PG8_WAIT_L(n) asm volatile("s_waitcnt lgkmcnt(" #n ")" ::: "memory")
; #define PG8_BAR __builtin_amdgcn_s_barrier()
; template <class Epi, class Sched>
; __device__ __forceinline__ void gemm_phase(LAS unsigned char* lds, const Sched& S, const Epi& E) {
;     ...
;             PG8_LDB(B0, 0, 0); PG8_LDB(B1, 0, 1); PG8_SCHED; PG8_LDA(At, 0, 0); PG8_STAGE(PG8_SA(1, 1), a1, vA[1]);
;             PG8_WAIT_V(8); PG8_WAIT_L(0); PG8_BAR; PG8_MMA(0, 0, At, B0); PG8_MMA(0, 1, At, B1); PG8_BAR2; PG8_SCHED;
;             if constexpr (Sched::GATHER) { if (last && has_next) {
;                 int tz = threadIdx.x; asm volatile("" : "+v"(tz));
; #pragma unroll
;                 for (int i = 0; i < 2; ++i) { int R, C; stage_rc(tz * 16 + i * 8192, R, C);
; #pragma unroll
;                     for (int h = 0; h < 2; ++h) vA[h][i] = (unsigned)(lidx[h * HALF + R] * RP + C * 2); } } }
;             PG8_LDA(At, 0, 1); PG8_STAGE(PG8_SB(0, 0), b2, voffB); PG8_STAGE(PG8_SB(0, 1), b2 + hstep, voffB); PG8_STAGE(PG8_SA(0, 0), a2, vA[0]);
;             PG8_WAIT_V(8); PG8_WAIT_L(0); PG8_BAR; PG8_MMA(1, 0, At, B0); PG8_MMA(1, 1, At, B1); PG8_BAR2; PG8_SCHED;
;             PG8_LDB(B0, 1, 0); PG8_LDB(B1, 1, 1); PG8_SCHED; PG8_LDA(At, 1, 0); PG8_STAGE(PG8_SA(0, 1), a2, vA[1]);
;             PG8_WAIT_V(8); PG8_WAIT_L(0); PG8_BAR; PG8_MMA(0, 0, At, B0); PG8_MMA(0, 1, At, B1); PG8_BAR2; PG8_SCHED;
;             PG8_LDA(At, 1, 1); PG8_STAGE(PG8_SB(1, 0), b3, voffB); PG8_STAGE(PG8_SB(1, 1), b3 + hstep, voffB); PG8_STAGE(PG8_SA(1, 0), a3, vA[0]);
;             PG8_WAIT_V(8); PG8_WAIT_L(0); PG8_BAR; PG8_MMA(1, 0, At, B0); PG8_MMA(1, 1, At, B1); PG8_BAR2; PG8_SCHED;
	s_setprio 1
	s_waitcnt lgkmcnt(0)
	s_nop 1
	v_mfma_scale_f32_16x16x128_f8f6f4 v[110:113], v[2:9], v[198:205], v[110:113], v185, v185 op_sel_hi:[0,0,0]
	v_mfma_scale_f32_16x16x128_f8f6f4 v[106:109], v[10:17], v[198:205], v[106:109], v185, v185 op_sel_hi:[0,0,0]
	v_mfma_scale_f32_16x16x128_f8f6f4 v[102:105], v[2:9], v[214:221], v[102:105], v185, v185 op_sel_hi:[0,0,0]
	v_mfma_scale_f32_16x16x128_f8f6f4 v[98:101], v[10:17], v[214:221], v[98:101], v185, v185 op_sel_hi:[0,0,0]
	v_mfma_scale_f32_16x16x128_f8f6f4 v[78:81], v[2:9], v[222:229], v[78:81], v185, v185 op_sel_hi:[0,0,0]
	v_mfma_scale_f32_16x16x128_f8f6f4 v[74:77], v[10:17], v[222:229], v[74:77], v185, v185 op_sel_hi:[0,0,0]
	v_mfma_scale_f32_16x16x128_f8f6f4 v[70:73], v[2:9], v[230:237], v[70:73], v185, v185 op_sel_hi:[0,0,0]
	v_mfma_scale_f32_16x16x128_f8f6f4 v[66:69], v[10:17], v[230:237], v[66:69], v185, v185 op_sel_hi:[0,0,0]
	s_setprio 0
	s_setprio 1
	s_nop 1
	v_mfma_scale_f32_16x16x128_f8f6f4 v[94:97], v[18:25], v[198:205], v[94:97], v185, v185 op_sel_hi:[0,0,0]
	v_mfma_scale_f32_16x16x128_f8f6f4 v[90:93], v[26:33], v[198:205], v[90:93], v185, v185 op_sel_hi:[0,0,0]
	v_mfma_scale_f32_16x16x128_f8f6f4 v[86:89], v[18:25], v[214:221], v[86:89], v185, v185 op_sel_hi:[0,0,0]
	v_mfma_scale_f32_16x16x128_f8f6f4 v[82:85], v[26:33], v[214:221], v[82:85], v185, v185 op_sel_hi:[0,0,0]
	v_mfma_scale_f32_16x16x128_f8f6f4 v[62:65], v[18:25], v[222:229], v[62:65], v185, v185 op_sel_hi:[0,0,0]
	v_mfma_scale_f32_16x16x128_f8f6f4 v[58:61], v[26:33], v[222:229], v[58:61], v185, v185 op_sel_hi:[0,0,0]
	v_mfma_scale_f32_16x16x128_f8f6f4 v[54:57], v[18:25], v[230:237], v[54:57], v185, v185 op_sel_hi:[0,0,0]
	v_mfma_scale_f32_16x16x128_f8f6f4 v[50:53], v[26:33], v[230:237], v[50:53], v185, v185 op_sel_hi:[0,0,0]
	s_setprio 0
	s_barrier
	s_add_i32 s84, s84, 2
	s_addk_i32 s83, 0x100
.LBB0_807:
	s_add_i32 s30, s83, 0xffffff00
	s_add_i32 s31, s83, 0xffffff80
	s_and_b32 s30, s30, 0x780
	s_and_b32 s31, s31, 0x780
	s_add_u32 s34, s26, s31
	s_addc_u32 s35, s27, 0
	s_add_u32 s40, s28, s31
	s_addc_u32 s41, s29, 0
	s_and_b32 s31, s83, 0x780
	s_add_u32 s53, s26, s31
	v_add_u32_e32 v2, s77, v186
	v_add_u32_e32 v22, s78, v186
	s_addc_u32 s85, s27, 0
	ds_read_b128 v[10:13], v2
	ds_read_b128 v[14:17], v2 offset:1024
	ds_read_b128 v[26:29], v2 offset:2048
	ds_read_b128 v[30:33], v2 offset:3072
	ds_read_b128 v[2:5], v22
	ds_read_b128 v[6:9], v22 offset:1024
	ds_read_b128 v[18:21], v22 offset:2048
	ds_read_b128 v[22:25], v22 offset:3072
	s_add_u32 s36, s28, s31
	s_addc_u32 s37, s29, 0
	s_add_u32 s54, s26, s30
	s_addc_u32 s55, s27, 0
	s_add_i32 s87, s77, s47
	s_add_i32 m0, s69, 0xc000
	s_add_i32 s86, s69, 0xe000
	s_add_i32 s52, s87, 0x2000
	s_cmp_eq_u32 s84, 12
	s_cselect_b32 s35, s17, s35
	s_cselect_b32 s34, s15, s34
	s_cselect_b32 s31, s80, s85
	s_cselect_b32 s30, s39, s53
	s_cselect_b32 s41, s38, s41
	s_cselect_b32 s40, s25, s40
	v_mov_b32_e32 v178, v183
	s_nop 0
	global_load_lds_dwordx4 v178, s[54:55]
	v_mov_b32_e32 v178, v184
	s_mov_b32 m0, s86
	s_nop 0
	global_load_lds_dwordx4 v178, s[54:55]
	ds_read_b128 v[198:201], v188
	ds_read_b128 v[202:205], v188 offset:1024
	ds_read_b128 v[214:217], v188 offset:2048
	ds_read_b128 v[218:221], v188 offset:3072
	ds_read_b128 v[222:225], v188 offset:4096
	ds_read_b128 v[226:229], v188 offset:5120
	ds_read_b128 v[230:233], v188 offset:6144
	ds_read_b128 v[234:237], v188 offset:7168
	s_waitcnt vmcnt(8)
	s_waitcnt lgkmcnt(0)
	s_barrier
	s_setprio 1
	s_waitcnt lgkmcnt(0)
	s_nop 1
	v_mfma_scale_f32_16x16x128_f8f6f4 v[174:177], v[10:17], v[198:205], v[174:177], v185, v185 op_sel_hi:[0,0,0]
	v_mfma_scale_f32_16x16x128_f8f6f4 v[170:173], v[26:33], v[198:205], v[170:173], v185, v185 op_sel_hi:[0,0,0]
	v_mfma_scale_f32_16x16x128_f8f6f4 v[166:169], v[10:17], v[214:221], v[166:169], v185, v185 op_sel_hi:[0,0,0]
	v_mfma_scale_f32_16x16x128_f8f6f4 v[162:165], v[26:33], v[214:221], v[162:165], v185, v185 op_sel_hi:[0,0,0]
	v_mfma_scale_f32_16x16x128_f8f6f4 v[142:145], v[10:17], v[222:229], v[142:145], v185, v185 op_sel_hi:[0,0,0]
	v_mfma_scale_f32_16x16x128_f8f6f4 v[138:141], v[26:33], v[222:229], v[138:141], v185, v185 op_sel_hi:[0,0,0]
	v_mfma_scale_f32_16x16x128_f8f6f4 v[134:137], v[10:17], v[230:237], v[134:137], v185, v185 op_sel_hi:[0,0,0]
	v_mfma_scale_f32_16x16x128_f8f6f4 v[130:133], v[26:33], v[230:237], v[130:133], v185, v185 op_sel_hi:[0,0,0]
	s_setprio 0
	s_setprio 1
	s_nop 1
	v_mfma_scale_f32_16x16x128_f8f6f4 v[158:161], v[2:9], v[198:205], v[158:161], v185, v185 op_sel_hi:[0,0,0]
	v_mfma_scale_f32_16x16x128_f8f6f4 v[154:157], v[18:25], v[198:205], v[154:157], v185, v185 op_sel_hi:[0,0,0]
	v_mfma_scale_f32_16x16x128_f8f6f4 v[150:153], v[2:9], v[214:221], v[150:153], v185, v185 op_sel_hi:[0,0,0]
	v_mfma_scale_f32_16x16x128_f8f6f4 v[146:149], v[18:25], v[214:221], v[146:149], v185, v185 op_sel_hi:[0,0,0]
	v_mfma_scale_f32_16x16x128_f8f6f4 v[126:129], v[2:9], v[222:229], v[126:129], v185, v185 op_sel_hi:[0,0,0]
	v_mfma_scale_f32_16x16x128_f8f6f4 v[122:125], v[18:25], v[222:229], v[122:125], v185, v185 op_sel_hi:[0,0,0]
	v_mfma_scale_f32_16x16x128_f8f6f4 v[118:121], v[2:9], v[230:237], v[118:121], v185, v185 op_sel_hi:[0,0,0]
	v_mfma_scale_f32_16x16x128_f8f6f4 v[114:117], v[18:25], v[230:237], v[114:117], v185, v185 op_sel_hi:[0,0,0]
	s_setprio 0
	s_barrier
; #define PG8_STAGE(bufoff, gbase, voff) do { if constexpr (!(Sched::CRIP & 2)) _Pragma("unroll") for (int _i = 0; _i < 2; ++_i) { unsigned _o = (voff)[_i]; asm volatile("" : "+v"(_o)); \
;         __builtin_amdgcn_global_load_lds((const unsigned*)((const char*)(gbase) + _o), (LAS unsigned*)(lds + (bufoff) + ldsw + _i * 8192), 16, 0, 0); } } while (0)
; #define PG8_LDA(dst, b, h) do { if constexpr (!(Sched::CRIP & 4)) _Pragma("unroll") for (int m = 0; m < 4; ++m) dst[m] = PG8_CAT(*(const LAS i32x4*)(lds + PG8_SA(b, h) + aoff + m * 2048), *(const LAS i32x4*)(lds + PG8_SA(b, h) + aoff + m * 2048 + 1024)); } while (0)
; #define PG8_LDB(dst, b, h) do { if constexpr (!(Sched::CRIP & 4)) _Pragma("unroll") for (int n = 0; n < 2; ++n) dst[n] = PG8_CAT(*(const LAS i32x4*)(lds + PG8_SB(b, h) + boff + n * 2048), *(const LAS i32x4*)(lds + PG8_SB(b, h) + boff + n * 2048 + 1024)); } while (0)
; #define PG8_WAIT_V(n) asm volatile("s_waitcnt vmcnt(" #n ")" ::: "memory")
; #define PG8_WAIT_L(n) asm volatile("s_waitcnt lgkmcnt(" #n ")" ::: "memory")
; #define PG8_BAR __builtin_amdgcn_s_barrier()
; #define PG8_SCHED __builtin_amdgcn_sched_barrier(0)
; template <class Epi, class Sched>
; __device__ __forceinline__ void gemm_phase(LAS unsigned char* lds, const Sched& S, const Epi& E) {
;     ...
;             PG8_LDA(At, 0, 1); PG8_STAGE(PG8_SB(0, 0), b2, voffB); PG8_STAGE(PG8_SB(0, 1), b2 + hstep, voffB); PG8_STAGE(PG8_SA(0, 0), a2, vA[0]);
;             PG8_WAIT_V(8); PG8_WAIT_L(0); PG8_BAR; PG8_MMA(1, 0, At, B0); PG8_MMA(1, 1, At, B1); PG8_BAR2; PG8_SCHED;
;             PG8_LDB(B0, 1, 0); PG8_LDB(B1, 1, 1); PG8_SCHED; PG8_LDA(At, 1, 0); PG8_STAGE(PG8_SA(0, 1), a2, vA[1]);
;             PG8_WAIT_V(8); PG8_WAIT_L(0); PG8_BAR; PG8_MMA(0, 0, At, B0); PG8_MMA(0, 1, At, B1); PG8_BAR2; PG8_SCHED;
	v_mov_b32_e32 v178, v1
	s_mov_b32 m0, s87
	s_cselect_b32 s36, s81, s36
	global_load_lds_dwordx4 v178, s[40:41]
	v_mov_b32_e32 v178, v180
	s_mov_b32 m0, s52
	s_cselect_b32 s37, s82, s37
	global_load_lds_dwordx4 v178, s[40:41]
	s_add_u32 s40, s40, 0x40000
	v_mov_b32_e32 v178, v1
	s_addc_u32 s41, s41, 0
	s_add_i32 s52, s78, s47
	s_mov_b32 m0, s52
	s_nop 0
	global_load_lds_dwordx4 v178, s[40:41]
	v_mov_b32_e32 v178, v180
	s_add_i32 m0, s52, 0x2000
	s_nop 0
	global_load_lds_dwordx4 v178, s[40:41]
	v_mov_b32_e32 v178, v181
	s_mov_b32 m0, s69
	s_nop 0
	global_load_lds_dwordx4 v178, s[34:35]
	v_mov_b32_e32 v178, v182
	s_mov_b32 m0, s70
	s_nop 0
	global_load_lds_dwordx4 v178, s[34:35]
	ds_read_b128 v[198:201], v188 offset:16384
	ds_read_b128 v[202:205], v188 offset:17408
	ds_read_b128 v[214:217], v188 offset:18432
	ds_read_b128 v[218:221], v188 offset:19456
	ds_read_b128 v[222:225], v188 offset:20480
	ds_read_b128 v[226:229], v188 offset:21504
	ds_read_b128 v[230:233], v188 offset:22528
	ds_read_b128 v[234:237], v188 offset:23552
	s_waitcnt vmcnt(8)
	s_waitcnt lgkmcnt(0)
	s_barrier
	s_setprio 1
	s_waitcnt lgkmcnt(0)
	s_nop 1
	v_mfma_scale_f32_16x16x128_f8f6f4 v[110:113], v[10:17], v[198:205], v[110:113], v185, v185 op_sel_hi:[0,0,0]
	v_mfma_scale_f32_16x16x128_f8f6f4 v[106:109], v[26:33], v[198:205], v[106:109], v185, v185 op_sel_hi:[0,0,0]
	v_mfma_scale_f32_16x16x128_f8f6f4 v[102:105], v[10:17], v[214:221], v[102:105], v185, v185 op_sel_hi:[0,0,0]
	v_mfma_scale_f32_16x16x128_f8f6f4 v[98:101], v[26:33], v[214:221], v[98:101], v185, v185 op_sel_hi:[0,0,0]
	v_mfma_scale_f32_16x16x128_f8f6f4 v[78:81], v[10:17], v[222:229], v[78:81], v185, v185 op_sel_hi:[0,0,0]
	v_mfma_scale_f32_16x16x128_f8f6f4 v[74:77], v[26:33], v[222:229], v[74:77], v185, v185 op_sel_hi:[0,0,0]
	v_mfma_scale_f32_16x16x128_f8f6f4 v[70:73], v[10:17], v[230:237], v[70:73], v185, v185 op_sel_hi:[0,0,0]
	v_mfma_scale_f32_16x16x128_f8f6f4 v[66:69], v[26:33], v[230:237], v[66:69], v185, v185 op_sel_hi:[0,0,0]
	s_setprio 0
	s_setprio 1
	s_nop 1
	v_mfma_scale_f32_16x16x128_f8f6f4 v[94:97], v[2:9], v[198:205], v[94:97], v185, v185 op_sel_hi:[0,0,0]
	v_mfma_scale_f32_16x16x128_f8f6f4 v[90:93], v[18:25], v[198:205], v[90:93], v185, v185 op_sel_hi:[0,0,0]
	v_mfma_scale_f32_16x16x128_f8f6f4 v[86:89], v[2:9], v[214:221], v[86:89], v185, v185 op_sel_hi:[0,0,0]
	v_mfma_scale_f32_16x16x128_f8f6f4 v[82:85], v[18:25], v[214:221], v[82:85], v185, v185 op_sel_hi:[0,0,0]
	v_mfma_scale_f32_16x16x128_f8f6f4 v[62:65], v[2:9], v[222:229], v[62:65], v185, v185 op_sel_hi:[0,0,0]
	v_mfma_scale_f32_16x16x128_f8f6f4 v[58:61], v[18:25], v[222:229], v[58:61], v185, v185 op_sel_hi:[0,0,0]
	v_mfma_scale_f32_16x16x128_f8f6f4 v[54:57], v[2:9], v[230:237], v[54:57], v185, v185 op_sel_hi:[0,0,0]
	v_mfma_scale_f32_16x16x128_f8f6f4 v[50:53], v[18:25], v[230:237], v[50:53], v185, v185 op_sel_hi:[0,0,0]
	s_setprio 0
	s_barrier
	s_add_i32 s40, 0, 0x18000
	s_add_i32 s41, 0, 0x1c000
	v_add_u32_e32 v14, s40, v186
	v_add_u32_e32 v30, s41, v186
	ds_read_b128 v[2:5], v14
	ds_read_b128 v[6:9], v14 offset:1024
	ds_read_b128 v[10:13], v14 offset:2048
	ds_read_b128 v[14:17], v14 offset:3072
	ds_read_b128 v[18:21], v30
	ds_read_b128 v[22:25], v30 offset:1024
	ds_read_b128 v[26:29], v30 offset:2048
	ds_read_b128 v[30:33], v30 offset:3072
	v_mov_b32_e32 v178, v183
	s_mov_b32 m0, s71
	s_nop 0
	global_load_lds_dwordx4 v178, s[34:35]
	v_mov_b32_e32 v178, v184
	s_mov_b32 m0, s72
	s_nop 0
	global_load_lds_dwordx4 v178, s[34:35]
	ds_read_b128 v[198:201], v188 offset:32768
	ds_read_b128 v[202:205], v188 offset:33792
	ds_read_b128 v[214:217], v188 offset:34816
	ds_read_b128 v[218:221], v188 offset:35840
	ds_read_b128 v[222:225], v188 offset:36864
	ds_read_b128 v[226:229], v188 offset:37888
	ds_read_b128 v[230:233], v188 offset:38912
	ds_read_b128 v[234:237], v188 offset:39936
	s_waitcnt vmcnt(8)
	s_waitcnt lgkmcnt(0)
	s_barrier
; #define PG8_STAGE(bufoff, gbase, voff) do { if constexpr (!(Sched::CRIP & 2)) _Pragma("unroll") for (int _i = 0; _i < 2; ++_i) { unsigned _o = (voff)[_i]; asm volatile("" : "+v"(_o)); \
;         __builtin_amdgcn_global_load_lds((const unsigned*)((const char*)(gbase) + _o), (LAS unsigned*)(lds + (bufoff) + ldsw + _i * 8192), 16, 0, 0); } } while (0)
; #define PG8_LDA(dst, b, h) do { if constexpr (!(Sched::CRIP & 4)) _Pragma("unroll") for (int m = 0; m < 4; ++m) dst[m] = PG8_CAT(*(const LAS i32x4*)(lds + PG8_SA(b, h) + aoff + m * 2048), *(const LAS i32x4*)(lds + PG8_SA(b, h) + aoff + m * 2048 + 1024)); } while (0)
; #define PG8_WAIT_V(n) asm volatile("s_waitcnt vmcnt(" #n ")" ::: "memory")
; #define PG8_WAIT_L(n) asm volatile("s_waitcnt lgkmcnt(" #n ")" ::: "memory")
; #define PG8_BAR __builtin_amdgcn_s_barrier()
; #define PG8_SCHED __builtin_amdgcn_sched_barrier(0)
; template <class Epi, class Sched>
; __device__ __forceinline__ void gemm_phase(LAS unsigned char* lds, const Sched& S, const Epi& E) {
;     ...
;             PG8_LDA(At, 1, 1); PG8_STAGE(PG8_SB(1, 0), b3, voffB); PG8_STAGE(PG8_SB(1, 1), b3 + hstep, voffB); PG8_STAGE(PG8_SA(1, 0), a3, vA[0]);
;             PG8_WAIT_V(8); PG8_WAIT_L(0); PG8_BAR; PG8_MMA(1, 0, At, B0); PG8_MMA(1, 1, At, B1); PG8_BAR2; PG8_SCHED;
;             if constexpr (Sched::GATHER) { if (t == 0 && has_next && tid < 256) lidx[tid] = (tid < nxt.avalid) ? gi : 0; }
;         }
;         if constexpr (F8) asm volatile("s_nop 15\n\ts_nop 15" ::: "memory");
;         if (wr == 0) PG8_BAR;
	s_setprio 1
	s_waitcnt lgkmcnt(0)
	s_nop 1
	v_mfma_scale_f32_16x16x128_f8f6f4 v[174:177], v[2:9], v[198:205], v[174:177], v185, v185 op_sel_hi:[0,0,0]
	v_mfma_scale_f32_16x16x128_f8f6f4 v[170:173], v[10:17], v[198:205], v[170:173], v185, v185 op_sel_hi:[0,0,0]
	v_mfma_scale_f32_16x16x128_f8f6f4 v[166:169], v[2:9], v[214:221], v[166:169], v185, v185 op_sel_hi:[0,0,0]
	v_mfma_scale_f32_16x16x128_f8f6f4 v[162:165], v[10:17], v[214:221], v[162:165], v185, v185 op_sel_hi:[0,0,0]
	v_mfma_scale_f32_16x16x128_f8f6f4 v[142:145], v[2:9], v[222:229], v[142:145], v185, v185 op_sel_hi:[0,0,0]
	v_mfma_scale_f32_16x16x128_f8f6f4 v[138:141], v[10:17], v[222:229], v[138:141], v185, v185 op_sel_hi:[0,0,0]
	v_mfma_scale_f32_16x16x128_f8f6f4 v[134:137], v[2:9], v[230:237], v[134:137], v185, v185 op_sel_hi:[0,0,0]
	v_mfma_scale_f32_16x16x128_f8f6f4 v[130:133], v[10:17], v[230:237], v[130:133], v185, v185 op_sel_hi:[0,0,0]
	s_setprio 0
	s_setprio 1
	s_nop 1
	v_mfma_scale_f32_16x16x128_f8f6f4 v[158:161], v[18:25], v[198:205], v[158:161], v185, v185 op_sel_hi:[0,0,0]
	v_mfma_scale_f32_16x16x128_f8f6f4 v[154:157], v[26:33], v[198:205], v[154:157], v185, v185 op_sel_hi:[0,0,0]
	v_mfma_scale_f32_16x16x128_f8f6f4 v[150:153], v[18:25], v[214:221], v[150:153], v185, v185 op_sel_hi:[0,0,0]
	v_mfma_scale_f32_16x16x128_f8f6f4 v[146:149], v[26:33], v[214:221], v[146:149], v185, v185 op_sel_hi:[0,0,0]
	v_mfma_scale_f32_16x16x128_f8f6f4 v[126:129], v[18:25], v[222:229], v[126:129], v185, v185 op_sel_hi:[0,0,0]
	v_mfma_scale_f32_16x16x128_f8f6f4 v[122:125], v[26:33], v[222:229], v[122:125], v185, v185 op_sel_hi:[0,0,0]
	v_mfma_scale_f32_16x16x128_f8f6f4 v[118:121], v[18:25], v[230:237], v[118:121], v185, v185 op_sel_hi:[0,0,0]
	v_mfma_scale_f32_16x16x128_f8f6f4 v[114:117], v[26:33], v[230:237], v[114:117], v185, v185 op_sel_hi:[0,0,0]
	s_setprio 0
	s_barrier
	v_mov_b32_e32 v178, v1
	s_add_i32 s34, s40, s47
	s_mov_b32 m0, s34
	s_nop 0
	global_load_lds_dwordx4 v178, s[36:37]
	v_mov_b32_e32 v178, v180
	s_add_i32 m0, s34, 0x2000
	s_add_u32 s34, s36, 0x40000
	global_load_lds_dwordx4 v178, s[36:37]
	s_addc_u32 s35, s37, 0
	v_mov_b32_e32 v178, v1
	s_add_i32 s36, s41, s47
	s_mov_b32 m0, s36
	s_nop 0
	global_load_lds_dwordx4 v178, s[34:35]
	v_mov_b32_e32 v178, v180
	s_add_i32 m0, s36, 0x2000
	s_nop 0
	global_load_lds_dwordx4 v178, s[34:35]
	v_mov_b32_e32 v178, v181
	s_mov_b32 m0, s74
	s_nop 0
	global_load_lds_dwordx4 v178, s[30:31]
	v_mov_b32_e32 v178, v182
	s_mov_b32 m0, s75
	s_nop 0
	global_load_lds_dwordx4 v178, s[30:31]
	ds_read_b128 v[198:201], v188 offset:49152
	ds_read_b128 v[202:205], v188 offset:50176
	ds_read_b128 v[214:217], v188 offset:51200
	ds_read_b128 v[218:221], v188 offset:52224
	ds_read_b128 v[222:225], v188 offset:53248
	ds_read_b128 v[226:229], v188 offset:54272
	ds_read_b128 v[230:233], v188 offset:55296
	ds_read_b128 v[234:237], v188 offset:56320
	s_waitcnt vmcnt(8)
	s_waitcnt lgkmcnt(0)
	s_barrier
	s_setprio 1
	s_waitcnt lgkmcnt(0)
	s_nop 1
	v_mfma_scale_f32_16x16x128_f8f6f4 v[110:113], v[2:9], v[198:205], v[110:113], v185, v185 op_sel_hi:[0,0,0]
	v_mfma_scale_f32_16x16x128_f8f6f4 v[106:109], v[10:17], v[198:205], v[106:109], v185, v185 op_sel_hi:[0,0,0]
	v_mfma_scale_f32_16x16x128_f8f6f4 v[102:105], v[2:9], v[214:221], v[102:105], v185, v185 op_sel_hi:[0,0,0]
	v_mfma_scale_f32_16x16x128_f8f6f4 v[98:101], v[10:17], v[214:221], v[98:101], v185, v185 op_sel_hi:[0,0,0]
	v_mfma_scale_f32_16x16x128_f8f6f4 v[78:81], v[2:9], v[222:229], v[78:81], v185, v185 op_sel_hi:[0,0,0]
	v_mfma_scale_f32_16x16x128_f8f6f4 v[74:77], v[10:17], v[222:229], v[74:77], v185, v185 op_sel_hi:[0,0,0]
	v_mfma_scale_f32_16x16x128_f8f6f4 v[70:73], v[2:9], v[230:237], v[70:73], v185, v185 op_sel_hi:[0,0,0]
	v_mfma_scale_f32_16x16x128_f8f6f4 v[66:69], v[10:17], v[230:237], v[66:69], v185, v185 op_sel_hi:[0,0,0]
	s_setprio 0
	s_setprio 1
	s_nop 1
	v_mfma_scale_f32_16x16x128_f8f6f4 v[94:97], v[18:25], v[198:205], v[94:97], v185, v185 op_sel_hi:[0,0,0]
	v_mfma_scale_f32_16x16x128_f8f6f4 v[90:93], v[26:33], v[198:205], v[90:93], v185, v185 op_sel_hi:[0,0,0]
	v_mfma_scale_f32_16x16x128_f8f6f4 v[86:89], v[18:25], v[214:221], v[86:89], v185, v185 op_sel_hi:[0,0,0]
	v_mfma_scale_f32_16x16x128_f8f6f4 v[82:85], v[26:33], v[214:221], v[82:85], v185, v185 op_sel_hi:[0,0,0]
	v_mfma_scale_f32_16x16x128_f8f6f4 v[62:65], v[18:25], v[222:229], v[62:65], v185, v185 op_sel_hi:[0,0,0]
	v_mfma_scale_f32_16x16x128_f8f6f4 v[58:61], v[26:33], v[222:229], v[58:61], v185, v185 op_sel_hi:[0,0,0]
	v_mfma_scale_f32_16x16x128_f8f6f4 v[54:57], v[18:25], v[230:237], v[54:57], v185, v185 op_sel_hi:[0,0,0]
	v_mfma_scale_f32_16x16x128_f8f6f4 v[50:53], v[26:33], v[230:237], v[50:53], v185, v185 op_sel_hi:[0,0,0]
	s_setprio 0
	s_barrier
	s_add_i32 s84, s84, 2
	s_addk_i32 s83, 0x100
	s_cmp_gt_u32 s84, 13
	s_cbranch_scc0 .LBB0_807
	s_nop 15
	s_nop 15
	s_and_b64 vcc, exec, s[8:9]
	s_cbranch_vccz .LBB0_810
	s_barrier
